# 4-bit v rows stored with the byte's two sign bits rotated so the gather needs one rotate instead of two shifts per dword (same values, same 4-bit storage)
# speedup vs baseline: 1.0109x; 1.0032x over previous
.LBB0_59:
	s_waitcnt vmcnt(0)
	v_mov_b32_e32 v8, v100
	v_mov_b32_e32 v9, v101
	v_mov_b32_e32 v10, v102
	v_mov_b32_e32 v11, v103
	v_mov_b32_e32 v4, v104
	v_mov_b32_e32 v5, v105
	v_mov_b32_e32 v6, v106
	v_mov_b32_e32 v7, v107
	v_mov_b32_e32 v12, v108
	v_mov_b32_e32 v13, v109
	v_mov_b32_e32 v14, v110
	v_mov_b32_e32 v15, v111
	v_mov_b32_e32 v0, v112
	v_mov_b32_e32 v1, v113
	v_mov_b32_e32 v2, v114
	v_mov_b32_e32 v3, v115
	v_add_u32_e32 v116, s86, v16
	v_cmp_ge_i32_e32 vcc, s22, v116
	v_lshl_add_u64 v[118:119], v[22:23], 0, s[14:15]
	s_nop 0
	v_cndmask_b32_e32 v118, v22, v118, vcc
	v_cndmask_b32_e32 v119, v23, v119, vcc
	global_load_dwordx4 v[100:103], v[118:119], off
	global_load_dwordx4 v[104:107], v[118:119], off offset:16
	global_load_dwordx4 v[108:111], v[118:119], off offset:32
	global_load_dwordx4 v[112:115], v[118:119], off offset:48
	v_mul_f32_e32 v19, v9, v9
	v_mov_b32_e32 v38, v11
	v_mov_b32_e32 v39, v4
	v_fmac_f32_e32 v19, v8, v8
	v_pk_mul_f32 v[38:39], v[38:39], v[38:39]
	v_fmac_f32_e32 v19, v10, v10
	v_mov_b32_e32 v40, v5
	v_mov_b32_e32 v41, v6
	v_add_f32_e32 v19, v19, v38
	v_pk_mul_f32 v[40:41], v[40:41], v[40:41]
	v_add_f32_e32 v19, v19, v39
	v_add_f32_e32 v19, v19, v40
	v_add_f32_e32 v19, v19, v41
	v_fmac_f32_e32 v19, v7, v7
	v_fmac_f32_e32 v19, v12, v12
	v_mov_b32_e32 v42, v15
	v_mov_b32_e32 v43, v0
	v_mov_b32_e32 v44, v1
	v_mov_b32_e32 v45, v2
	v_fmac_f32_e32 v19, v13, v13
	v_pk_mov_b32 v[42:43], v[42:43], v[44:45] op_sel:[1,0]
	v_fmac_f32_e32 v19, v14, v14
	v_pk_mul_f32 v[42:43], v[42:43], v[42:43]
	v_fmac_f32_e32 v19, v15, v15
	v_add_f32_e32 v19, v19, v42
	v_pk_mul_f32 v[46:47], v[2:3], v[2:3]
	v_add_f32_e32 v19, v19, v43
	v_add_f32_e32 v19, v19, v46
	v_add_f32_e32 v19, v19, v47
	ds_bpermute_b32 v38, v32, v19
	v_mov_b32_e32 v39, v15
	v_mov_b32_e32 v41, v0
	v_mov_b32_e32 v0, v5
	v_mov_b32_e32 v43, v2
	s_waitcnt lgkmcnt(0)
	v_add_f32_e32 v19, v19, v38
	ds_bpermute_b32 v38, v33, v19
	v_mov_b32_e32 v42, v6
	v_mov_b32_e32 v44, v8
	v_mov_b32_e32 v45, v12
	v_mov_b32_e32 v12, v9
	s_waitcnt lgkmcnt(0)
	v_add_f32_e32 v19, v19, v38
	ds_bpermute_b32 v38, v34, v19
	s_waitcnt lgkmcnt(0)
	v_add_f32_e32 v19, v19, v38
	ds_bpermute_b32 v38, v35, v19
	s_waitcnt lgkmcnt(0)
	v_add_f32_e32 v19, v19, v38
	ds_bpermute_b32 v40, v36, v19
	v_mov_b32_e32 v38, v11
	s_waitcnt lgkmcnt(0)
	v_add_f32_e32 v11, v19, v40
	ds_bpermute_b32 v15, v37, v11
	v_mov_b32_e32 v40, v4
	s_waitcnt lgkmcnt(0)
	v_add_f32_e32 v4, v11, v15
	v_mul_f32_e32 v4, 0x3a800000, v4
	v_mul_f32_e32 v5, 0x4f800000, v4
	v_cmp_gt_f32_e32 vcc, s3, v4
	s_nop 1
	v_cndmask_b32_e32 v4, v4, v5, vcc
	v_sqrt_f32_e32 v5, v4
	s_nop 0
	v_add_u32_e32 v2, -1, v5
	v_add_u32_e32 v6, 1, v5
	v_fma_f32 v8, -v2, v5, v4
	v_fma_f32 v11, -v6, v5, v4
	v_cmp_ge_f32_e64 s[8:9], 0, v8
	s_nop 1
	v_cndmask_b32_e64 v2, v5, v2, s[8:9]
	v_cmp_lt_f32_e64 s[8:9], 0, v11
	s_nop 1
	v_cndmask_b32_e64 v2, v2, v6, s[8:9]
	v_mul_f32_e32 v5, 0x37800000, v2
	v_cndmask_b32_e32 v2, v2, v5, vcc
	v_cmp_class_f32_e32 vcc, v4, v17
	s_nop 1
	v_cndmask_b32_e32 v2, v2, v4, vcc
	v_mul_f32_e32 v5, 0x3f89999a, v2
	v_div_scale_f32 v2, s[8:9], v5, v5, 1.0
	v_rcp_f32_e32 v4, v2
	v_div_scale_f32 v6, vcc, 1.0, v5, 1.0
	v_fma_f32 v8, -v2, v4, 1.0
	v_fmac_f32_e32 v4, v8, v4
	v_mul_f32_e32 v8, v6, v4
	v_fma_f32 v9, -v2, v8, v6
	v_fmac_f32_e32 v8, v9, v4
	v_fma_f32 v2, -v2, v8, v6
	v_div_fmas_f32 v2, v2, v4, v8
	v_div_fixup_f32 v2, v2, v5, 1.0
	v_cmp_lt_f32_e32 vcc, 0, v5
	s_nop 1
	v_cndmask_b32_e32 v4, 0, v2, vcc
	v_pk_mul_f32 v[8:9], v[38:39], v[4:5] op_sel_hi:[1,0]
	v_pk_mul_f32 v[38:39], v[40:41], v[4:5] op_sel_hi:[1,0]
	v_cmp_gt_f32_e64 s[8:9], |v8|, s16
	v_pk_mul_f32 v[40:41], v[0:1], v[4:5] op_sel_hi:[1,0]
	v_pk_mul_f32 v[0:1], v[42:43], v[4:5] op_sel_hi:[1,0]
	v_cndmask_b32_e64 v2, 0, 1, s[8:9]
	v_cmp_gt_f32_e64 s[8:9], |v8|, 0.5
	v_pk_mul_f32 v[42:43], v[44:45], v[4:5] op_sel_hi:[1,0]
	v_cmp_gt_f32_e64 vcc, |v8|, s17
	v_cndmask_b32_e64 v6, 0, 1, s[8:9]
	v_cmp_gt_f32_e64 s[8:9], |v38|, s16
	v_addc_co_u32_e32 v2, vcc, v2, v6, vcc
	s_nop 0
	v_cndmask_b32_e64 v15, 0, 1, s[8:9]
	v_cmp_gt_f32_e64 s[8:9], |v38|, 0.5
	v_pk_mul_f32 v[12:13], v[12:13], v[4:5] op_sel_hi:[1,0]
	v_cmp_gt_f32_e64 vcc, |v42|, s17
	v_cndmask_b32_e64 v19, 0, 1, s[8:9]
	v_cmp_gt_f32_e64 s[8:9], |v42|, s16
	v_lshrrev_b32_e32 v51, 28, v43
	v_lshrrev_b32_e32 v52, 28, v42
	v_cndmask_b32_e64 v11, 0, 1, s[8:9]
	v_cmp_gt_f32_e64 s[8:9], |v42|, 0.5
	s_nop 1
	v_cndmask_b32_e64 v44, 0, 1, s[8:9]
	v_cmp_gt_f32_e64 s[8:9], |v42|, s19
	v_addc_co_u32_e32 v6, vcc, v11, v44, vcc
	s_nop 0
	v_cndmask_b32_e64 v45, 0, 1, s[8:9]
	v_cmp_gt_f32_e64 s[8:9], |v43|, s16
	v_cmp_gt_f32_e64 vcc, |v43|, s17
	v_and_b32_e32 v44, 8, v51
	v_cndmask_b32_e64 v46, 0, 1, s[8:9]
	v_cmp_gt_f32_e64 s[8:9], |v43|, 0.5
	s_nop 1
	v_cndmask_b32_e64 v47, 0, 1, s[8:9]
	v_cmp_gt_f32_e64 s[8:9], |v43|, s19
	v_addc_co_u32_e32 v11, vcc, v46, v47, vcc
	s_nop 0
	v_cndmask_b32_e64 v48, 0, 1, s[8:9]
	v_cmp_gt_f32_e64 s[8:9], |v42|, s20
	v_cmp_gt_f32_e64 vcc, |v12|, s17
	v_and_b32_e32 v46, 8, v52
	v_cndmask_b32_e64 v49, 0, 1, s[8:9]
	v_cmp_gt_f32_e64 s[8:9], |v43|, s20
	s_nop 1
	v_cndmask_b32_e64 v50, 0, 1, s[8:9]
	v_cmp_gt_f32_e64 s[8:9], |v12|, s16
	s_nop 1
	v_cndmask_b32_e64 v53, 0, 1, s[8:9]
	v_cmp_gt_f32_e64 s[8:9], |v12|, 0.5
	s_nop 1
	v_cndmask_b32_e64 v54, 0, 1, s[8:9]
	v_cmp_gt_f32_e64 s[8:9], |v12|, s19
	v_addc_co_u32_e32 v47, vcc, v53, v54, vcc
	s_nop 0
	v_cndmask_b32_e64 v55, 0, 1, s[8:9]
	v_cmp_gt_f32_e64 s[8:9], |v13|, s16
	v_cmp_gt_f32_e64 vcc, |v13|, s17
	s_nop 0
	v_cndmask_b32_e64 v56, 0, 1, s[8:9]
	v_cmp_gt_f32_e64 s[8:9], |v13|, 0.5
	s_nop 1
	v_cndmask_b32_e64 v57, 0, 1, s[8:9]
	v_addc_co_u32_e32 v51, vcc, v56, v57, vcc
	v_cmp_gt_f32_e64 vcc, |v42|, s18
	v_cmp_gt_f32_e64 s[8:9], |v13|, s19
	s_nop 0
	v_addc_co_u32_e32 v6, vcc, v6, v45, vcc
	v_cmp_gt_f32_e64 vcc, |v43|, s18
	v_cndmask_b32_e64 v58, 0, 1, s[8:9]
	v_cmp_gt_f32_e64 s[8:9], |v12|, s20
	v_addc_co_u32_e32 v11, vcc, v11, v48, vcc
	v_cmp_gt_f32_e64 vcc, |v12|, s18
	s_nop 1
	v_addc_co_u32_e32 v45, vcc, v47, v55, vcc
	v_cmp_gt_f32_e64 vcc, |v43|, s21
	v_cndmask_b32_e64 v43, 0, 1, s[8:9]
	v_cmp_gt_f32_e64 s[8:9], |v13|, s20
	v_addc_co_u32_e32 v11, vcc, v11, v50, vcc
	v_cmp_gt_f32_e64 vcc, |v42|, s21
	v_or_b32_e32 v11, v11, v44
	v_cndmask_b32_e64 v44, 0, 1, s[8:9]
	v_addc_co_u32_e32 v6, vcc, v6, v49, vcc
	v_cmp_gt_f32_e64 vcc, |v13|, s18
	v_or_b32_e32 v6, v6, v46
	s_nop 0
	v_addc_co_u32_e32 v42, vcc, v51, v58, vcc
	v_cmp_gt_f32_e64 vcc, |v13|, s21
	v_lshrrev_b32_e32 v13, 28, v13
	v_and_b32_e32 v13, 8, v13
	v_addc_co_u32_e32 v42, vcc, v42, v44, vcc
	v_or_b32_e32 v13, v42, v13
	v_cmp_gt_f32_e64 vcc, |v12|, s21
	v_lshrrev_b32_e32 v12, 28, v12
	v_lshlrev_b32_e32 v13, 4, v13
	v_addc_co_u32_e32 v43, vcc, v45, v43, vcc
	v_and_b32_e32 v12, 8, v12
	v_or_b32_e32 v13, v11, v13
	v_mov_b32_e32 v11, v14
	v_or_b32_e32 v12, v43, v12
	v_pk_mul_f32 v[10:11], v[10:11], v[4:5] op_sel_hi:[1,0]
	v_lshlrev_b32_e32 v12, 4, v12
	v_cmp_gt_f32_e64 s[8:9], |v10|, s16
	v_or_b32_e32 v6, v6, v12
	v_cmp_gt_f32_e64 vcc, |v10|, s17
	v_cndmask_b32_e64 v12, 0, 1, s[8:9]
	v_cmp_gt_f32_e64 s[8:9], |v10|, 0.5
	s_nop 1
	v_cndmask_b32_e64 v14, 0, 1, s[8:9]
	v_cmp_gt_f32_e64 s[8:9], |v10|, s19
	v_addc_co_u32_e32 v12, vcc, v12, v14, vcc
	s_nop 0
	v_cndmask_b32_e64 v14, 0, 1, s[8:9]
	v_cmp_gt_f32_e64 s[8:9], |v11|, s16
	v_cmp_gt_f32_e64 vcc, |v11|, s17
	s_nop 0
	v_cndmask_b32_e64 v42, 0, 1, s[8:9]
	v_cmp_gt_f32_e64 s[8:9], |v11|, 0.5
	s_nop 1
	v_cndmask_b32_e64 v43, 0, 1, s[8:9]
	v_addc_co_u32_e32 v42, vcc, v42, v43, vcc
	v_cmp_gt_f32_e64 vcc, |v10|, s18
	v_cmp_gt_f32_e64 s[8:9], |v11|, s19
	s_nop 0
	v_addc_co_u32_e32 v12, vcc, v12, v14, vcc
	v_cndmask_b32_e64 v43, 0, 1, s[8:9]
	v_cmp_gt_f32_e64 vcc, |v11|, s18
	v_cmp_gt_f32_e64 s[8:9], |v10|, s20
	s_nop 0
	v_addc_co_u32_e32 v14, vcc, v42, v43, vcc
	v_cndmask_b32_e64 v42, 0, 1, s[8:9]
	v_cmp_gt_f32_e64 s[8:9], |v11|, s20
	v_cmp_gt_f32_e64 vcc, |v11|, s21
	v_lshrrev_b32_e32 v11, 28, v11
	v_cndmask_b32_e64 v43, 0, 1, s[8:9]
	v_addc_co_u32_e32 v14, vcc, v14, v43, vcc
	v_cmp_gt_f32_e64 vcc, |v10|, s21
	v_lshrrev_b32_e32 v10, 28, v10
	v_and_b32_e32 v10, 8, v10
	v_addc_co_u32_e32 v12, vcc, v12, v42, vcc
	v_or_b32_e32 v10, v12, v10
	v_lshlrev_b32_e32 v10, 8, v10
	v_cmp_gt_f32_e64 s[8:9], |v9|, s16
	v_and_b32_e32 v11, 8, v11
	v_or_b32_e32 v6, v6, v10
	v_cndmask_b32_e64 v10, 0, 1, s[8:9]
	v_cmp_gt_f32_e64 s[8:9], |v9|, 0.5
	v_or_b32_e32 v11, v14, v11
	v_cmp_gt_f32_e64 vcc, |v9|, s17
	v_cndmask_b32_e64 v12, 0, 1, s[8:9]
	v_cmp_gt_f32_e64 s[8:9], |v9|, s19
	v_lshlrev_b32_e32 v11, 8, v11
	v_addc_co_u32_e32 v10, vcc, v10, v12, vcc
	v_cndmask_b32_e64 v12, 0, 1, s[8:9]
	v_cmp_gt_f32_e64 s[8:9], |v8|, s19
	v_or_b32_e32 v11, v13, v11
	v_cmp_gt_f32_e64 vcc, |v8|, s18
	v_cndmask_b32_e64 v13, 0, 1, s[8:9]
	v_cmp_gt_f32_e64 s[8:9], |v8|, s20
	v_addc_co_u32_e32 v2, vcc, v2, v13, vcc
	v_cmp_gt_f32_e64 vcc, |v9|, s18
	s_nop 1
	v_addc_co_u32_e32 v10, vcc, v10, v12, vcc
	v_cndmask_b32_e64 v12, 0, 1, s[8:9]
	v_cmp_gt_f32_e64 s[8:9], |v9|, s20
	v_cmp_gt_f32_e64 vcc, |v9|, s21
	v_lshrrev_b32_e32 v9, 28, v9
	v_cndmask_b32_e64 v13, 0, 1, s[8:9]
	v_addc_co_u32_e32 v10, vcc, v10, v13, vcc
	v_cmp_gt_f32_e64 vcc, |v8|, s21
	v_lshrrev_b32_e32 v8, 28, v8
	v_and_b32_e32 v8, 8, v8
	v_addc_co_u32_e32 v2, vcc, v2, v12, vcc
	v_or_b32_e32 v2, v2, v8
	v_and_b32_e32 v9, 8, v9
	v_lshlrev_b32_e32 v2, 12, v2
	v_cmp_gt_f32_e64 s[8:9], |v39|, s16
	v_or_b32_e32 v9, v10, v9
	v_or_b32_e32 v2, v6, v2
	v_cndmask_b32_e64 v6, 0, 1, s[8:9]
	v_cmp_gt_f32_e64 s[8:9], |v39|, 0.5
	v_lshlrev_b32_e32 v8, 12, v9
	v_cmp_gt_f32_e64 vcc, |v39|, s17
	v_cndmask_b32_e64 v9, 0, 1, s[8:9]
	v_cmp_gt_f32_e64 s[8:9], |v39|, s19
	v_addc_co_u32_e32 v6, vcc, v6, v9, vcc
	v_cmp_gt_f32_e64 vcc, |v38|, s17
	v_cndmask_b32_e64 v10, 0, 1, s[8:9]
	v_cmp_gt_f32_e64 s[8:9], |v38|, s19
	v_addc_co_u32_e32 v9, vcc, v15, v19, vcc
	v_or_b32_e32 v8, v11, v8
	v_cndmask_b32_e64 v11, 0, 1, s[8:9]
	v_cmp_gt_f32_e64 vcc, |v38|, s18
	v_cmp_gt_f32_e64 s[8:9], |v38|, s20
	s_nop 0
	v_addc_co_u32_e32 v9, vcc, v9, v11, vcc
	v_cmp_gt_f32_e64 vcc, |v39|, s18
	s_nop 1
	v_addc_co_u32_e32 v6, vcc, v6, v10, vcc
	v_cndmask_b32_e64 v10, 0, 1, s[8:9]
	v_cmp_gt_f32_e64 s[8:9], |v39|, s20
	v_cmp_gt_f32_e64 vcc, |v39|, s21
	s_nop 0
	v_cndmask_b32_e64 v11, 0, 1, s[8:9]
	v_addc_co_u32_e32 v6, vcc, v6, v11, vcc
	v_cmp_gt_f32_e64 vcc, |v38|, s21
	v_lshrrev_b32_e32 v11, 28, v38
	v_and_b32_e32 v11, 8, v11
	v_addc_co_u32_e32 v9, vcc, v9, v10, vcc
	v_lshrrev_b32_e32 v10, 28, v39
	v_and_b32_e32 v10, 8, v10
	v_or_b32_sdwa v6, v6, v10 dst_sel:WORD_1 dst_unused:UNUSED_PAD src0_sel:DWORD src1_sel:DWORD
	v_cmp_gt_f32_e64 s[8:9], |v40|, s16
	v_or_b32_sdwa v9, v9, v11 dst_sel:WORD_1 dst_unused:UNUSED_PAD src0_sel:DWORD src1_sel:DWORD
	v_or_b32_e32 v6, v8, v6
	v_cndmask_b32_e64 v8, 0, 1, s[8:9]
	v_cmp_gt_f32_e64 s[8:9], |v41|, s16
	v_or_b32_e32 v2, v2, v9
	v_cmp_gt_f32_e64 vcc, |v41|, s17
	v_cndmask_b32_e64 v9, 0, 1, s[8:9]
	v_cmp_gt_f32_e64 s[8:9], |v40|, 0.5
	s_nop 1
	v_cndmask_b32_e64 v10, 0, 1, s[8:9]
	v_cmp_gt_f32_e64 s[8:9], |v41|, 0.5
	s_nop 1
	v_cndmask_b32_e64 v11, 0, 1, s[8:9]
	v_addc_co_u32_e32 v9, vcc, v9, v11, vcc
	v_cmp_gt_f32_e64 vcc, |v40|, s17
	v_cmp_gt_f32_e64 s[8:9], |v41|, s19
	s_nop 0
	v_addc_co_u32_e32 v8, vcc, v8, v10, vcc
	v_cndmask_b32_e64 v10, 0, 1, s[8:9]
	v_cmp_gt_f32_e64 s[8:9], |v40|, s19
	v_cmp_gt_f32_e64 vcc, |v40|, s18
	s_nop 0
	v_cndmask_b32_e64 v11, 0, 1, s[8:9]
	v_addc_co_u32_e32 v8, vcc, v8, v11, vcc
	v_cmp_gt_f32_e64 vcc, |v41|, s18
	v_cmp_gt_f32_e64 s[8:9], |v40|, s20
	s_nop 0
	v_addc_co_u32_e32 v9, vcc, v9, v10, vcc
	v_cndmask_b32_e64 v10, 0, 1, s[8:9]
	v_cmp_gt_f32_e64 s[8:9], |v41|, s20
	v_cmp_gt_f32_e64 vcc, |v41|, s21
	s_nop 0
	v_cndmask_b32_e64 v11, 0, 1, s[8:9]
	v_addc_co_u32_e32 v9, vcc, v9, v11, vcc
	v_cmp_gt_f32_e64 vcc, |v40|, s21
	v_lshrrev_b32_e32 v11, 28, v40
	v_and_b32_e32 v11, 8, v11
	v_addc_co_u32_e32 v8, vcc, v8, v10, vcc
	v_lshrrev_b32_e32 v10, 28, v41
	v_and_b32_e32 v10, 8, v10
	v_or_b32_e32 v8, v8, v11
	v_or_b32_e32 v9, v9, v10
	v_lshlrev_b32_e32 v8, 20, v8
	v_cmp_gt_f32_e64 s[8:9], |v0|, s16
	v_lshlrev_b32_e32 v9, 20, v9
	v_or_b32_e32 v2, v2, v8
	v_cndmask_b32_e64 v8, 0, 1, s[8:9]
	v_cmp_gt_f32_e64 s[8:9], |v1|, s16
	v_or_b32_e32 v6, v6, v9
	v_cmp_gt_f32_e64 vcc, |v1|, s17
	v_cndmask_b32_e64 v9, 0, 1, s[8:9]
	v_cmp_gt_f32_e64 s[8:9], |v0|, 0.5
	s_nop 1
	v_cndmask_b32_e64 v10, 0, 1, s[8:9]
	v_cmp_gt_f32_e64 s[8:9], |v1|, 0.5
	s_nop 1
	v_cndmask_b32_e64 v11, 0, 1, s[8:9]
	v_addc_co_u32_e32 v9, vcc, v9, v11, vcc
	v_cmp_gt_f32_e64 vcc, |v0|, s17
	v_cmp_gt_f32_e64 s[8:9], |v1|, s19
	s_nop 0
	v_addc_co_u32_e32 v8, vcc, v8, v10, vcc
	v_cndmask_b32_e64 v10, 0, 1, s[8:9]
	v_cmp_gt_f32_e64 s[8:9], |v0|, s19
	v_cmp_gt_f32_e64 vcc, |v0|, s18
	s_nop 0
	v_cndmask_b32_e64 v11, 0, 1, s[8:9]
	v_addc_co_u32_e32 v8, vcc, v8, v11, vcc
	v_cmp_gt_f32_e64 vcc, |v1|, s18
	v_cmp_gt_f32_e64 s[8:9], |v0|, s20
	s_nop 0
	v_addc_co_u32_e32 v9, vcc, v9, v10, vcc
	v_cndmask_b32_e64 v10, 0, 1, s[8:9]
	v_cmp_gt_f32_e64 s[8:9], |v1|, s20
	v_cmp_gt_f32_e64 vcc, |v1|, s21
	v_lshrrev_b32_e32 v1, 28, v1
	v_cndmask_b32_e64 v11, 0, 1, s[8:9]
	v_addc_co_u32_e32 v9, vcc, v9, v11, vcc
	v_cmp_gt_f32_e64 vcc, |v0|, s21
	v_lshrrev_b32_e32 v0, 28, v0
	v_and_b32_e32 v0, 8, v0
	v_addc_co_u32_e32 v8, vcc, v8, v10, vcc
	v_and_b32_e32 v1, 8, v1
	v_or_b32_sdwa v0, v8, v0 dst_sel:BYTE_3 dst_unused:UNUSED_PAD src0_sel:DWORD src1_sel:DWORD
	v_or_b32_sdwa v1, v9, v1 dst_sel:BYTE_3 dst_unused:UNUSED_PAD src0_sel:DWORD src1_sel:DWORD
	v_or_b32_e32 v8, v2, v0
	v_mov_b32_e32 v2, v7
	v_or_b32_e32 v6, v6, v1
	v_pk_mul_f32 v[0:1], v[2:3], v[4:5] op_sel_hi:[1,0]
	s_nop 0
	v_cmp_gt_f32_e64 s[8:9], |v1|, s16
	v_cmp_gt_f32_e64 vcc, |v0|, s17
	s_nop 0
	v_cndmask_b32_e64 v2, 0, 1, s[8:9]
	v_cmp_gt_f32_e64 s[8:9], |v0|, s16
	s_nop 1
	v_cndmask_b32_e64 v3, 0, 1, s[8:9]
	v_cmp_gt_f32_e64 s[8:9], |v1|, 0.5
	s_nop 1
	v_cndmask_b32_e64 v4, 0, 1, s[8:9]
	v_cmp_gt_f32_e64 s[8:9], |v0|, 0.5
	s_nop 1
	v_cndmask_b32_e64 v7, 0, 1, s[8:9]
	v_addc_co_u32_e32 v3, vcc, v3, v7, vcc
	v_cmp_gt_f32_e64 vcc, |v1|, s17
	v_cmp_gt_f32_e64 s[8:9], |v0|, s19
	s_nop 0
	v_addc_co_u32_e32 v2, vcc, v2, v4, vcc
	v_cndmask_b32_e64 v4, 0, 1, s[8:9]
	v_cmp_gt_f32_e64 s[8:9], |v1|, s19
	v_cmp_gt_f32_e64 vcc, |v1|, s18
	s_nop 0
	v_cndmask_b32_e64 v7, 0, 1, s[8:9]
	v_addc_co_u32_e32 v2, vcc, v2, v7, vcc
	v_cmp_gt_f32_e64 vcc, |v0|, s18
	v_cmp_gt_f32_e64 s[8:9], |v1|, s20
	s_nop 0
	v_addc_co_u32_e32 v3, vcc, v3, v4, vcc
	v_cndmask_b32_e64 v4, 0, 1, s[8:9]
	v_cmp_gt_f32_e64 s[8:9], |v0|, s20
	v_cmp_gt_f32_e64 vcc, |v0|, s21
	v_and_b32_e32 v0, 0x80000000, v0
	v_cndmask_b32_e64 v7, 0, 1, s[8:9]
	v_addc_co_u32_e32 v3, vcc, v3, v7, vcc
	v_cmp_gt_f32_e64 vcc, |v1|, s21
	v_lshlrev_b32_e32 v3, 28, v3
	v_and_b32_e32 v1, 0x80000000, v1
	v_addc_co_u32_e32 v2, vcc, v2, v4, vcc
	v_lshlrev_b32_e32 v2, 28, v2
	v_or_b32_e32 v1, v2, v1
	v_or_b32_e32 v0, v3, v0
	v_or_b32_e32 v1, v6, v1
	v_or_b32_e32 v0, v8, v0
	v_and_b32_e32 v60, 0x88888888, v0
	v_and_b32_e32 v61, 0x88888888, v1
	v_and_b32_e32 v0, 0x77777777, v0
	v_and_b32_e32 v1, 0x77777777, v1
	v_alignbit_b32 v60, v60, v60, 28
	v_alignbit_b32 v61, v61, v61, 28
	v_or_b32_e32 v0, v0, v60
	v_or_b32_e32 v1, v1, v61
	global_store_dwordx2 v[20:21], v[0:1], off
	s_and_saveexec_b64 s[8:9], s[6:7]
	s_cbranch_execz .LBB0_58
	v_ashrrev_i32_e32 v19, 31, v18
	v_lshl_add_u64 v[0:1], v[18:19], 2, s[88:89]
	global_store_dword v[0:1], v5, off
	s_branch .LBB0_58

.LBB0_763:
	s_cmpk_eq_i32 s58, 0x80
	s_cselect_b64 s[12:13], -1, 0
	ds_bpermute_b32 v84, v93, v92
	s_and_b64 vcc, s[12:13], s[48:49]
	v_cndmask_b32_e32 v104, v0, v94, vcc
	v_ashrrev_i32_e32 v105, 31, v104
	s_and_b32 s12, s58, 0x70
	v_lshlrev_b64 v[104:105], 9, v[104:105]
	v_lshl_add_u64 v[104:105], s[94:95], 0, v[104:105]
	s_lshl_b32 s36, s12, 2
	s_waitcnt lgkmcnt(0)
	v_ashrrev_i32_e32 v85, 31, v84
	v_lshl_add_u64 v[104:105], v[104:105], 0, s[36:37]
	v_lshl_add_u64 v[84:85], v[84:85], 3, s[8:9]
	v_lshl_add_u64 v[104:105], v[104:105], 0, v[144:145]
	global_load_dwordx2 v[84:85], v[84:85], off
	s_nop 0
	global_load_dword v86, v[72:73], off
	global_load_dword v92, v[104:105], off
	s_waitcnt vmcnt(11)
	v_dot8_i32_i4 v87, v8, v1, 0
	v_dot8_i32_i4 v104, v8, v88, 0
	v_dot8_i32_i4 v87, v9, v89, v87
	v_dot8_i32_i4 v104, v9, v90, v104
	s_waitcnt vmcnt(10)
	v_dot8_i32_i4 v9, v10, v88, 0
	v_dot8_i32_i4 v9, v11, v90, v9
	v_lshl_add_u32 v87, v87, 4, v104
	v_dot8_i32_i4 v8, v10, v1, 0
	v_dot8_i32_i4 v8, v11, v89, v8
	s_add_i32 s58, s58, 16
	v_lshl_add_u64 v[72:73], v[72:73], 0, 64
	s_waitcnt vmcnt(2)
	v_mul_f32_e32 v85, v91, v85
	v_lshl_add_u32 v104, v8, 4, v9
	v_dot8_i32_i4 v8, v12, v1, 0
	v_dot8_i32_i4 v9, v12, v88, 0
	v_dot8_i32_i4 v8, v13, v89, v8
	v_dot8_i32_i4 v9, v13, v90, v9
	s_waitcnt vmcnt(0)
	v_readlane_b32 s12, v92, 0
	v_readlane_b32 s28, v92, 8
	v_readlane_b32 s30, v92, 9
	v_lshl_add_u32 v105, v8, 4, v9
	v_dot8_i32_i4 v8, v14, v1, 0
	v_dot8_i32_i4 v9, v14, v88, 0
	v_dot8_i32_i4 v8, v15, v89, v8
	v_dot8_i32_i4 v9, v15, v90, v9
	s_ashr_i32 s13, s12, 31
	v_readlane_b32 s14, v92, 1
	s_ashr_i32 s29, s28, 31
	v_lshl_add_u32 v106, v8, 4, v9
	v_dot8_i32_i4 v8, v16, v1, 0
	v_dot8_i32_i4 v9, v16, v88, 0
	v_dot8_i32_i4 v8, v17, v89, v8
	v_dot8_i32_i4 v9, v17, v90, v9
	s_ashr_i32 s31, s30, 31
	v_readlane_b32 s34, v92, 10
	s_lshl_b64 s[12:13], s[12:13], 9
	v_lshl_add_u32 v107, v8, 4, v9
	v_dot8_i32_i4 v8, v18, v1, 0
	v_dot8_i32_i4 v9, v18, v88, 0
	v_dot8_i32_i4 v8, v19, v89, v8
	v_dot8_i32_i4 v9, v19, v90, v9
	s_ashr_i32 s15, s14, 31
	v_readlane_b32 s16, v92, 2
	s_lshl_b64 s[28:29], s[28:29], 9
	v_lshl_add_u32 v108, v8, 4, v9
	v_dot8_i32_i4 v8, v20, v1, 0
	v_dot8_i32_i4 v9, v20, v88, 0
	v_dot8_i32_i4 v8, v21, v89, v8
	v_dot8_i32_i4 v9, v21, v90, v9
	s_lshl_b64 s[30:31], s[30:31], 9
	s_ashr_i32 s35, s34, 31
	v_readlane_b32 s38, v92, 11
	v_lshl_add_u32 v109, v8, 4, v9
	v_dot8_i32_i4 v8, v22, v1, 0
	v_dot8_i32_i4 v9, v22, v88, 0
	v_dot8_i32_i4 v8, v23, v89, v8
	v_dot8_i32_i4 v9, v23, v90, v9
	s_lshl_b64 s[14:15], s[14:15], 9
	s_ashr_i32 s17, s16, 31
	v_readlane_b32 s18, v92, 3
	v_lshl_add_u32 v110, v8, 4, v9
	v_dot8_i32_i4 v8, v24, v1, 0
	v_dot8_i32_i4 v9, v24, v88, 0
	v_dot8_i32_i4 v8, v25, v89, v8
	v_dot8_i32_i4 v9, v25, v90, v9
	s_lshl_b64 s[34:35], s[34:35], 9
	s_ashr_i32 s39, s38, 31
	s_nop 0
	v_lshl_add_u32 v111, v8, 4, v9
	v_dot8_i32_i4 v8, v38, v1, 0
	v_dot8_i32_i4 v9, v38, v88, 0
	v_dot8_i32_i4 v8, v39, v89, v8
	v_dot8_i32_i4 v9, v39, v90, v9
	v_permlane32_swap_b32 v87, v111
	s_nop 1
	v_lshl_add_u32 v112, v8, 4, v9
	v_dot8_i32_i4 v8, v50, v1, 0
	v_dot8_i32_i4 v9, v50, v88, 0
	v_dot8_i32_i4 v8, v51, v89, v8
	v_dot8_i32_i4 v9, v51, v90, v9
	s_waitcnt lgkmcnt(0)
	v_add_u32_e32 v87, v87, v111
	v_permlane32_swap_b32 v104, v112
	v_lshl_add_u32 v113, v8, 4, v9
	v_dot8_i32_i4 v8, v48, v1, 0
	v_dot8_i32_i4 v9, v48, v88, 0
	v_dot8_i32_i4 v8, v49, v89, v8
	v_dot8_i32_i4 v9, v49, v90, v9
	s_waitcnt lgkmcnt(0)
	v_add_u32_e32 v104, v104, v112
	v_permlane32_swap_b32 v105, v113
	v_lshl_add_u32 v114, v8, 4, v9
	v_dot8_i32_i4 v8, v46, v1, 0
	v_dot8_i32_i4 v9, v46, v88, 0
	v_dot8_i32_i4 v8, v47, v89, v8
	v_dot8_i32_i4 v9, v47, v90, v9
	s_waitcnt lgkmcnt(0)
	v_add_u32_e32 v105, v105, v113
	v_permlane32_swap_b32 v106, v114
	v_lshl_add_u32 v115, v8, 4, v9
	v_dot8_i32_i4 v8, v44, v1, 0
	v_dot8_i32_i4 v9, v44, v88, 0
	v_dot8_i32_i4 v8, v45, v89, v8
	v_dot8_i32_i4 v9, v45, v90, v9
	s_waitcnt lgkmcnt(0)
	v_add_u32_e32 v106, v106, v114
	v_permlane32_swap_b32 v107, v115
	v_lshl_add_u32 v116, v8, 4, v9
	v_dot8_i32_i4 v8, v42, v1, 0
	v_dot8_i32_i4 v9, v42, v88, 0
	v_dot8_i32_i4 v8, v43, v89, v8
	v_dot8_i32_i4 v9, v43, v90, v9
	s_waitcnt lgkmcnt(0)
	v_add_u32_e32 v107, v107, v115
	v_permlane32_swap_b32 v108, v116
	v_lshl_add_u32 v117, v8, 4, v9
	v_dot8_i32_i4 v8, v40, v1, 0
	v_dot8_i32_i4 v9, v40, v88, 0
	v_dot8_i32_i4 v8, v41, v89, v8
	v_dot8_i32_i4 v9, v41, v90, v9
	s_waitcnt lgkmcnt(0)
	v_add_u32_e32 v108, v108, v116
	v_permlane32_swap_b32 v109, v117
	v_lshl_add_u32 v118, v8, 4, v9
	s_waitcnt lgkmcnt(0)
	v_add_u32_e32 v109, v109, v117
	v_permlane32_swap_b32 v110, v118
	v_readlane_b32 s50, v92, 12
	s_lshl_b64 s[16:17], s[16:17], 9
	s_ashr_i32 s19, s18, 31
	s_waitcnt lgkmcnt(0)
	v_add_u32_e32 v110, v110, v118
	v_permlane16_swap_b32 v87, v107
	v_readlane_b32 s20, v92, 4
	s_add_u32 s66, s28, s62
	s_addc_u32 s67, s29, s63
	global_load_dwordx2 v[24:25], v121, s[66:67]
	s_add_u32 s66, s30, s62
	s_addc_u32 s67, s31, s63
	global_load_dwordx2 v[38:39], v121, s[66:67]
	s_waitcnt lgkmcnt(0)
	v_add_u32_e32 v87, v87, v107
	v_permlane16_swap_b32 v104, v108
	s_lshl_b64 s[38:39], s[38:39], 9
	s_ashr_i32 s51, s50, 31
	v_readlane_b32 s52, v92, 13
	s_waitcnt lgkmcnt(0)
	v_add_u32_e32 v104, v104, v108
	v_permlane16_swap_b32 v105, v109
	s_lshl_b64 s[18:19], s[18:19], 9
	s_ashr_i32 s21, s20, 31
	v_readlane_b32 s22, v92, 5
	s_waitcnt lgkmcnt(0)
	v_add_u32_e32 v105, v105, v109
	v_permlane16_swap_b32 v106, v110
	s_add_u32 s66, s34, s62
	s_addc_u32 s67, s35, s63
	global_load_dwordx2 v[50:51], v121, s[66:67]
	s_lshl_b64 s[50:51], s[50:51], 9
	s_ashr_i32 s53, s52, 31
	s_waitcnt lgkmcnt(0)
	v_add_u32_e32 v106, v106, v110
	v_cndmask_b32_e64 v107, v87, v105, s[44:45]
	v_cndmask_b32_e64 v87, v105, v87, s[44:45]
	s_nop 0
	v_readlane_b32 s54, v92, 14
	s_lshl_b64 s[20:21], s[20:21], 9
	s_ashr_i32 s23, s22, 31
	v_readlane_b32 s24, v92, 6
	s_waitcnt lgkmcnt(0)
	v_add_u32_dpp v87, v107, v87 row_ror:8 row_mask:0xf bank_mask:0xf
	v_cndmask_b32_e64 v105, v104, v106, s[44:45]
	s_nop 1
	v_cndmask_b32_e64 v104, v106, v104, s[44:45]
	s_lshl_b64 s[52:53], s[52:53], 9
	s_ashr_i32 s55, s54, 31
	v_readlane_b32 s56, v92, 15
	s_waitcnt lgkmcnt(0)
	v_add_u32_dpp v104, v105, v104 row_ror:8 row_mask:0xf bank_mask:0xf
	v_cndmask_b32_e64 v105, v87, v104, s[46:47]
	v_cndmask_b32_e64 v87, v104, v87, s[46:47]
	s_nop 0
	v_mov_b32_dpp v104, v105 row_half_mirror row_mask:0xf bank_mask:0xf
	s_nop 1
	s_lshl_b64 s[22:23], s[22:23], 9
	s_ashr_i32 s25, s24, 31
	v_readlane_b32 s26, v92, 7
	s_lshl_b64 s[54:55], s[54:55], 9
	s_waitcnt lgkmcnt(0)
	v_add_u32_dpp v87, v104, v87 quad_perm:[3,2,1,0] row_mask:0xf bank_mask:0xf
	s_nop 1
	s_ashr_i32 s57, s56, 31
	s_lshl_b64 s[24:25], s[24:25], 9
	s_ashr_i32 s27, s26, 31
	s_lshl_b64 s[56:57], s[56:57], 9
	s_waitcnt lgkmcnt(0)
	v_add_u32_dpp v87, v87, v87 quad_perm:[2,3,0,1] row_mask:0xf bank_mask:0xf
	s_nop 1
	s_lshl_b64 s[26:27], s[26:27], 9
	s_waitcnt lgkmcnt(0)
	v_add_u32_dpp v87, v87, v87 quad_perm:[1,0,3,2] row_mask:0xf bank_mask:0xf
	v_cvt_f32_i32_e32 v87, v87
	v_add_f32_e32 v87, v95, v87
	v_mul_f32_e32 v85, v85, v87
	v_mul_f32_e32 v87, 0x3d372713, v85
	v_mul_f32_e32 v87, v85, v87
	v_fma_f32 v87, v85, v87, v85
	v_mul_f32_e32 v87, 0x3fcc422a, v87
	v_mul_f32_e32 v87, 0xbfb8aa3b, v87
	v_exp_f32_e32 v87, v87
	s_nop 0
	v_add_f32_e32 v87, 1.0, v87
	v_rcp_f32_e32 v87, v87
	s_nop 0
	v_pk_mul_f32 v[84:85], v[84:85], v[86:87]
	v_alignbit_b32 v224, v82, v82, 4
	v_pk_mul_f32 v[84:85], v[84:85], v[84:85] op_sel:[0,1] op_sel_hi:[1,0]
	v_cvt_f16_f32_e32 v120, v84
	v_and_b32_e32 v86, 0x7070707, v82
	v_readlane_b32 s36, v120, 0
	v_and_b32_e32 v87, 0x7070707, v224
	v_perm_b32 v86, s2, v205, v86
	v_perm_b32 v87, s2, v205, v87
	v_and_or_b32 v86, v82, s4, v86
	v_and_or_b32 v82, v224, s4, v87
	v_perm_b32 v87, v82, v86, s5
	v_perm_b32 v104, v82, v86, s33
	v_perm_b32 v105, v82, v86, s0
	v_perm_b32 v82, v82, v86, s1
	v_pk_fma_f16 v86, v87, s36, v103 op_sel_hi:[1,0,1]
	v_pk_fma_f16 v87, v104, s36, v102 op_sel_hi:[1,0,1]
	v_alignbit_b32 v225, v83, v83, 4
	v_pk_fma_f16 v82, v82, s36, v100 op_sel_hi:[1,0,1]
	v_and_b32_e32 v100, 0x7070707, v83
	v_and_b32_e32 v102, 0x7070707, v225
	v_perm_b32 v100, s2, v205, v100
	v_perm_b32 v102, s2, v205, v102
	v_and_or_b32 v100, v83, s4, v100
	v_and_or_b32 v83, v225, s4, v102
	v_perm_b32 v102, v83, v100, s5
	v_perm_b32 v103, v83, v100, s33
	v_perm_b32 v104, v83, v100, s0
	v_perm_b32 v83, v83, v100, s1
	v_readlane_b32 s59, v120, 4
	v_alignbit_b32 v224, v80, v80, 4
	v_pk_fma_f16 v101, v105, s36, v101 op_sel_hi:[1,0,1]
	v_pk_fma_f16 v99, v102, s36, v99 op_sel_hi:[1,0,1]
	v_pk_fma_f16 v98, v103, s36, v98 op_sel_hi:[1,0,1]
	v_pk_fma_f16 v97, v104, s36, v97 op_sel_hi:[1,0,1]
	v_pk_fma_f16 v83, v83, s36, v96 op_sel_hi:[1,0,1]
	v_and_b32_e32 v96, 0x7070707, v80
	v_and_b32_e32 v100, 0x7070707, v224
	v_perm_b32 v96, s2, v205, v96
	v_perm_b32 v100, s2, v205, v100
	v_and_or_b32 v96, v80, s4, v96
	v_and_or_b32 v80, v224, s4, v100
	v_perm_b32 v100, v80, v96, s5
	v_perm_b32 v102, v80, v96, s33
	v_perm_b32 v103, v80, v96, s0
	v_perm_b32 v80, v80, v96, s1
	v_pk_fma_f16 v86, v100, s59, v86 op_sel_hi:[1,0,1]
	v_alignbit_b32 v225, v81, v81, 4
	v_pk_fma_f16 v80, v80, s59, v82 op_sel_hi:[1,0,1]
	v_and_b32_e32 v82, 0x7070707, v81
	v_and_b32_e32 v100, 0x7070707, v225
	v_pk_fma_f16 v96, v103, s59, v101 op_sel_hi:[1,0,1]
	v_perm_b32 v82, s2, v205, v82
	v_perm_b32 v100, s2, v205, v100
	v_and_or_b32 v82, v81, s4, v82
	v_and_or_b32 v81, v225, s4, v100
	v_perm_b32 v100, v81, v82, s5
	v_pk_fma_f16 v87, v102, s59, v87 op_sel_hi:[1,0,1]
	v_perm_b32 v101, v81, v82, s33
	v_perm_b32 v102, v81, v82, s0
	v_perm_b32 v81, v81, v82, s1
	v_pk_fma_f16 v82, v100, s59, v99 op_sel_hi:[1,0,1]
	v_readlane_b32 s60, v120, 8
	v_alignbit_b32 v224, v78, v78, 4
	v_pk_fma_f16 v98, v101, s59, v98 op_sel_hi:[1,0,1]
	v_pk_fma_f16 v97, v102, s59, v97 op_sel_hi:[1,0,1]
	v_pk_fma_f16 v81, v81, s59, v83 op_sel_hi:[1,0,1]
	v_and_b32_e32 v85, 0x7070707, v78
	v_and_b32_e32 v99, 0x7070707, v224
	v_perm_b32 v85, s2, v205, v85
	v_perm_b32 v99, s2, v205, v99
	v_and_or_b32 v85, v78, s4, v85
	v_and_or_b32 v78, v224, s4, v99
	v_perm_b32 v99, v78, v85, s5
	v_perm_b32 v100, v78, v85, s33
	v_perm_b32 v101, v78, v85, s0
	v_perm_b32 v78, v78, v85, s1
	v_pk_fma_f16 v85, v99, s60, v86 op_sel_hi:[1,0,1]
	v_pk_fma_f16 v86, v100, s60, v87 op_sel_hi:[1,0,1]
	v_pk_fma_f16 v87, v101, s60, v96 op_sel_hi:[1,0,1]
	v_alignbit_b32 v225, v79, v79, 4
	v_pk_fma_f16 v78, v78, s60, v80 op_sel_hi:[1,0,1]
	v_and_b32_e32 v80, 0x7070707, v79
	v_and_b32_e32 v96, 0x7070707, v225
	v_perm_b32 v80, s2, v205, v80
	v_perm_b32 v96, s2, v205, v96
	v_and_or_b32 v80, v79, s4, v80
	v_and_or_b32 v79, v225, s4, v96
	v_perm_b32 v96, v79, v80, s5
	v_perm_b32 v100, v79, v80, s0
	v_perm_b32 v99, v79, v80, s33
	v_perm_b32 v79, v79, v80, s1
	v_pk_fma_f16 v80, v96, s60, v82 op_sel_hi:[1,0,1]
	v_pk_fma_f16 v96, v100, s60, v97 op_sel_hi:[1,0,1]
	v_readlane_b32 s36, v120, 12
	v_alignbit_b32 v224, v76, v76, 4
	v_pk_fma_f16 v82, v99, s60, v98 op_sel_hi:[1,0,1]
	v_pk_fma_f16 v79, v79, s60, v81 op_sel_hi:[1,0,1]
	v_and_b32_e32 v83, 0x7070707, v76
	v_and_b32_e32 v97, 0x7070707, v224
	v_perm_b32 v83, s2, v205, v83
	v_perm_b32 v97, s2, v205, v97
	v_and_or_b32 v83, v76, s4, v83
	v_and_or_b32 v76, v224, s4, v97
	v_perm_b32 v97, v76, v83, s5
	v_perm_b32 v98, v76, v83, s33
	v_perm_b32 v99, v76, v83, s0
	v_perm_b32 v76, v76, v83, s1
	v_pk_fma_f16 v83, v97, s36, v85 op_sel_hi:[1,0,1]
	v_pk_fma_f16 v85, v98, s36, v86 op_sel_hi:[1,0,1]
	v_pk_fma_f16 v86, v99, s36, v87 op_sel_hi:[1,0,1]
	v_alignbit_b32 v225, v77, v77, 4
	v_pk_fma_f16 v76, v76, s36, v78 op_sel_hi:[1,0,1]
	v_and_b32_e32 v78, 0x7070707, v77
	v_and_b32_e32 v87, 0x7070707, v225
	v_perm_b32 v78, s2, v205, v78
	v_perm_b32 v87, s2, v205, v87
	v_and_or_b32 v78, v77, s4, v78
	v_and_or_b32 v77, v225, s4, v87
	v_perm_b32 v87, v77, v78, s5
	v_perm_b32 v97, v77, v78, s33
	v_perm_b32 v98, v77, v78, s0
	v_perm_b32 v77, v77, v78, s1
	v_pk_fma_f16 v78, v87, s36, v80 op_sel_hi:[1,0,1]
	v_readlane_b32 s59, v120, 16
	v_alignbit_b32 v224, v74, v74, 4
	v_pk_fma_f16 v80, v97, s36, v82 op_sel_hi:[1,0,1]
	v_pk_fma_f16 v82, v98, s36, v96 op_sel_hi:[1,0,1]
	v_pk_fma_f16 v77, v77, s36, v79 op_sel_hi:[1,0,1]
	v_and_b32_e32 v81, 0x7070707, v74
	v_and_b32_e32 v87, 0x7070707, v224
	v_perm_b32 v81, s2, v205, v81
	v_perm_b32 v87, s2, v205, v87
	v_and_or_b32 v81, v74, s4, v81
	v_and_or_b32 v74, v224, s4, v87
	v_perm_b32 v87, v74, v81, s5
	v_perm_b32 v96, v74, v81, s33
	v_perm_b32 v97, v74, v81, s0
	v_perm_b32 v74, v74, v81, s1
	v_pk_fma_f16 v81, v87, s59, v83 op_sel_hi:[1,0,1]
	v_pk_fma_f16 v83, v96, s59, v85 op_sel_hi:[1,0,1]
	v_pk_fma_f16 v85, v97, s59, v86 op_sel_hi:[1,0,1]
	v_alignbit_b32 v225, v75, v75, 4
	v_pk_fma_f16 v74, v74, s59, v76 op_sel_hi:[1,0,1]
	v_and_b32_e32 v76, 0x7070707, v75
	v_and_b32_e32 v86, 0x7070707, v225
	v_perm_b32 v76, s2, v205, v76
	v_perm_b32 v86, s2, v205, v86
	v_and_or_b32 v76, v75, s4, v76
	v_and_or_b32 v75, v225, s4, v86
	v_perm_b32 v86, v75, v76, s5
	v_perm_b32 v87, v75, v76, s33
	v_perm_b32 v96, v75, v76, s0
	v_perm_b32 v75, v75, v76, s1
	v_pk_fma_f16 v76, v86, s59, v78 op_sel_hi:[1,0,1]
	v_pk_fma_f16 v78, v87, s59, v80 op_sel_hi:[1,0,1]
	v_pk_fma_f16 v80, v96, s59, v82 op_sel_hi:[1,0,1]
	v_readlane_b32 s60, v120, 20
	v_alignbit_b32 v224, v70, v70, 4
	v_pk_fma_f16 v75, v75, s59, v77 op_sel_hi:[1,0,1]
	v_and_b32_e32 v79, 0x7070707, v70
	v_and_b32_e32 v82, 0x7070707, v224
	v_perm_b32 v79, s2, v205, v79
	v_perm_b32 v82, s2, v205, v82
	v_and_or_b32 v79, v70, s4, v79
	v_and_or_b32 v70, v224, s4, v82
	v_perm_b32 v82, v70, v79, s5
	v_perm_b32 v86, v70, v79, s33
	v_perm_b32 v87, v70, v79, s0
	v_perm_b32 v70, v70, v79, s1
	v_pk_fma_f16 v79, v82, s60, v81 op_sel_hi:[1,0,1]
	v_pk_fma_f16 v81, v86, s60, v83 op_sel_hi:[1,0,1]
	v_alignbit_b32 v225, v71, v71, 4
	v_pk_fma_f16 v70, v70, s60, v74 op_sel_hi:[1,0,1]
	v_and_b32_e32 v74, 0x7070707, v71
	v_and_b32_e32 v83, 0x7070707, v225
	v_pk_fma_f16 v82, v87, s60, v85 op_sel_hi:[1,0,1]
	v_perm_b32 v74, s2, v205, v74
	v_perm_b32 v83, s2, v205, v83
	v_and_or_b32 v74, v71, s4, v74
	v_and_or_b32 v71, v225, s4, v83
	v_perm_b32 v83, v71, v74, s5
	v_perm_b32 v85, v71, v74, s33
	v_perm_b32 v86, v71, v74, s0
	v_perm_b32 v71, v71, v74, s1
	v_pk_fma_f16 v74, v83, s60, v76 op_sel_hi:[1,0,1]
	v_pk_fma_f16 v76, v85, s60, v78 op_sel_hi:[1,0,1]
	v_pk_fma_f16 v78, v86, s60, v80 op_sel_hi:[1,0,1]
	v_readlane_b32 s36, v120, 24
	v_alignbit_b32 v224, v68, v68, 4
	v_pk_fma_f16 v71, v71, s60, v75 op_sel_hi:[1,0,1]
	v_and_b32_e32 v77, 0x7070707, v68
	v_and_b32_e32 v80, 0x7070707, v224
	v_perm_b32 v77, s2, v205, v77
	v_perm_b32 v80, s2, v205, v80
	v_and_or_b32 v77, v68, s4, v77
	v_and_or_b32 v68, v224, s4, v80
	v_perm_b32 v80, v68, v77, s5
	v_perm_b32 v83, v68, v77, s33
	v_perm_b32 v85, v68, v77, s0
	v_perm_b32 v68, v68, v77, s1
	v_pk_fma_f16 v77, v80, s36, v79 op_sel_hi:[1,0,1]
	v_pk_fma_f16 v79, v83, s36, v81 op_sel_hi:[1,0,1]
	v_alignbit_b32 v225, v69, v69, 4
	v_pk_fma_f16 v68, v68, s36, v70 op_sel_hi:[1,0,1]
	v_and_b32_e32 v70, 0x7070707, v69
	v_and_b32_e32 v81, 0x7070707, v225
	v_pk_fma_f16 v80, v85, s36, v82 op_sel_hi:[1,0,1]
	v_perm_b32 v70, s2, v205, v70
	v_perm_b32 v81, s2, v205, v81
	v_and_or_b32 v70, v69, s4, v70
	v_and_or_b32 v69, v225, s4, v81
	v_perm_b32 v81, v69, v70, s5
	v_perm_b32 v82, v69, v70, s33
	v_perm_b32 v83, v69, v70, s0
	v_perm_b32 v69, v69, v70, s1
	v_pk_fma_f16 v70, v81, s36, v74 op_sel_hi:[1,0,1]
	v_pk_fma_f16 v74, v82, s36, v76 op_sel_hi:[1,0,1]
	v_pk_fma_f16 v76, v83, s36, v78 op_sel_hi:[1,0,1]
	v_readlane_b32 s59, v120, 28
	v_alignbit_b32 v224, v64, v64, 4
	v_pk_fma_f16 v69, v69, s36, v71 op_sel_hi:[1,0,1]
	v_and_b32_e32 v75, 0x7070707, v64
	v_and_b32_e32 v78, 0x7070707, v224
	v_perm_b32 v75, s2, v205, v75
	v_perm_b32 v78, s2, v205, v78
	v_and_or_b32 v75, v64, s4, v75
	v_and_or_b32 v64, v224, s4, v78
	v_perm_b32 v78, v64, v75, s5
	v_perm_b32 v81, v64, v75, s33
	v_perm_b32 v82, v64, v75, s0
	v_perm_b32 v64, v64, v75, s1
	v_pk_fma_f16 v75, v78, s59, v77 op_sel_hi:[1,0,1]
	v_pk_fma_f16 v77, v81, s59, v79 op_sel_hi:[1,0,1]
	v_alignbit_b32 v225, v65, v65, 4
	v_pk_fma_f16 v64, v64, s59, v68 op_sel_hi:[1,0,1]
	v_and_b32_e32 v68, 0x7070707, v65
	v_and_b32_e32 v79, 0x7070707, v225
	v_pk_fma_f16 v78, v82, s59, v80 op_sel_hi:[1,0,1]
	v_perm_b32 v68, s2, v205, v68
	v_perm_b32 v79, s2, v205, v79
	v_and_or_b32 v68, v65, s4, v68
	v_and_or_b32 v65, v225, s4, v79
	v_perm_b32 v79, v65, v68, s5
	v_perm_b32 v80, v65, v68, s33
	v_perm_b32 v81, v65, v68, s0
	v_perm_b32 v65, v65, v68, s1
	v_pk_fma_f16 v68, v79, s59, v70 op_sel_hi:[1,0,1]
	v_pk_fma_f16 v70, v80, s59, v74 op_sel_hi:[1,0,1]
	v_pk_fma_f16 v74, v81, s59, v76 op_sel_hi:[1,0,1]
	v_readlane_b32 s60, v120, 32
	v_alignbit_b32 v224, v62, v62, 4
	v_pk_fma_f16 v65, v65, s59, v69 op_sel_hi:[1,0,1]
	v_and_b32_e32 v71, 0x7070707, v62
	v_and_b32_e32 v76, 0x7070707, v224
	v_perm_b32 v71, s2, v205, v71
	v_perm_b32 v76, s2, v205, v76
	v_and_or_b32 v71, v62, s4, v71
	v_and_or_b32 v62, v224, s4, v76
	v_perm_b32 v76, v62, v71, s5
	v_perm_b32 v79, v62, v71, s33
	v_perm_b32 v80, v62, v71, s0
	v_perm_b32 v62, v62, v71, s1
	v_pk_fma_f16 v71, v76, s60, v75 op_sel_hi:[1,0,1]
	v_pk_fma_f16 v75, v79, s60, v77 op_sel_hi:[1,0,1]
	v_alignbit_b32 v225, v63, v63, 4
	v_pk_fma_f16 v62, v62, s60, v64 op_sel_hi:[1,0,1]
	v_and_b32_e32 v64, 0x7070707, v63
	v_and_b32_e32 v77, 0x7070707, v225
	v_pk_fma_f16 v76, v80, s60, v78 op_sel_hi:[1,0,1]
	v_perm_b32 v64, s2, v205, v64
	v_perm_b32 v77, s2, v205, v77
	v_and_or_b32 v64, v63, s4, v64
	v_and_or_b32 v63, v225, s4, v77
	v_perm_b32 v77, v63, v64, s5
	v_perm_b32 v78, v63, v64, s33
	v_perm_b32 v79, v63, v64, s0
	v_perm_b32 v63, v63, v64, s1
	v_pk_fma_f16 v64, v77, s60, v68 op_sel_hi:[1,0,1]
	v_pk_fma_f16 v68, v78, s60, v70 op_sel_hi:[1,0,1]
	v_pk_fma_f16 v70, v79, s60, v74 op_sel_hi:[1,0,1]
	v_readlane_b32 s36, v120, 36
	v_alignbit_b32 v224, v66, v66, 4
	v_pk_fma_f16 v63, v63, s60, v65 op_sel_hi:[1,0,1]
	v_and_b32_e32 v69, 0x7070707, v66
	v_and_b32_e32 v74, 0x7070707, v224
	v_perm_b32 v69, s2, v205, v69
	v_perm_b32 v74, s2, v205, v74
	v_and_or_b32 v69, v66, s4, v69
	v_and_or_b32 v66, v224, s4, v74
	v_perm_b32 v74, v66, v69, s5
	v_perm_b32 v77, v66, v69, s33
	v_perm_b32 v78, v66, v69, s0
	v_perm_b32 v66, v66, v69, s1
	v_pk_fma_f16 v69, v74, s36, v71 op_sel_hi:[1,0,1]
	v_pk_fma_f16 v71, v77, s36, v75 op_sel_hi:[1,0,1]
	v_alignbit_b32 v225, v67, v67, 4
	v_pk_fma_f16 v62, v66, s36, v62 op_sel_hi:[1,0,1]
	v_and_b32_e32 v66, 0x7070707, v67
	v_and_b32_e32 v75, 0x7070707, v225
	v_pk_fma_f16 v74, v78, s36, v76 op_sel_hi:[1,0,1]
	v_perm_b32 v66, s2, v205, v66
	v_perm_b32 v75, s2, v205, v75
	v_and_or_b32 v66, v67, s4, v66
	v_and_or_b32 v67, v225, s4, v75
	v_perm_b32 v76, v67, v66, s33
	v_perm_b32 v77, v67, v66, s0
	v_perm_b32 v75, v67, v66, s5
	v_perm_b32 v66, v67, v66, s1
	v_pk_fma_f16 v67, v76, s36, v68 op_sel_hi:[1,0,1]
	v_pk_fma_f16 v68, v77, s36, v70 op_sel_hi:[1,0,1]
	v_readlane_b32 s59, v120, 40
	v_alignbit_b32 v224, v60, v60, 4
	v_pk_fma_f16 v64, v75, s36, v64 op_sel_hi:[1,0,1]
	v_pk_fma_f16 v63, v66, s36, v63 op_sel_hi:[1,0,1]
	v_and_b32_e32 v66, 0x7070707, v60
	v_and_b32_e32 v70, 0x7070707, v224
	v_perm_b32 v66, s2, v205, v66
	v_perm_b32 v70, s2, v205, v70
	v_and_or_b32 v66, v60, s4, v66
	v_and_or_b32 v60, v224, s4, v70
	v_perm_b32 v70, v60, v66, s5
	v_perm_b32 v75, v60, v66, s33
	v_perm_b32 v76, v60, v66, s0
	v_perm_b32 v60, v60, v66, s1
	v_pk_fma_f16 v66, v70, s59, v69 op_sel_hi:[1,0,1]
	v_pk_fma_f16 v69, v75, s59, v71 op_sel_hi:[1,0,1]
	v_alignbit_b32 v225, v61, v61, 4
	v_pk_fma_f16 v60, v60, s59, v62 op_sel_hi:[1,0,1]
	v_and_b32_e32 v62, 0x7070707, v61
	v_and_b32_e32 v71, 0x7070707, v225
	v_pk_fma_f16 v70, v76, s59, v74 op_sel_hi:[1,0,1]
	v_perm_b32 v62, s2, v205, v62
	v_perm_b32 v71, s2, v205, v71
	v_and_or_b32 v62, v61, s4, v62
	v_and_or_b32 v61, v225, s4, v71
	v_perm_b32 v71, v61, v62, s5
	v_perm_b32 v74, v61, v62, s33
	v_perm_b32 v75, v61, v62, s0
	v_perm_b32 v61, v61, v62, s1
	v_pk_fma_f16 v62, v71, s59, v64 op_sel_hi:[1,0,1]
	v_pk_fma_f16 v64, v74, s59, v67 op_sel_hi:[1,0,1]
	v_pk_fma_f16 v67, v75, s59, v68 op_sel_hi:[1,0,1]
	v_readlane_b32 s60, v120, 44
	v_alignbit_b32 v224, v58, v58, 4
	v_pk_fma_f16 v61, v61, s59, v63 op_sel_hi:[1,0,1]
	v_and_b32_e32 v65, 0x7070707, v58
	v_and_b32_e32 v68, 0x7070707, v224
	v_perm_b32 v65, s2, v205, v65
	v_perm_b32 v68, s2, v205, v68
	v_and_or_b32 v65, v58, s4, v65
	v_and_or_b32 v58, v224, s4, v68
	v_perm_b32 v68, v58, v65, s5
	v_perm_b32 v71, v58, v65, s33
	v_perm_b32 v74, v58, v65, s0
	v_perm_b32 v58, v58, v65, s1
	v_pk_fma_f16 v65, v68, s60, v66 op_sel_hi:[1,0,1]
	v_pk_fma_f16 v66, v71, s60, v69 op_sel_hi:[1,0,1]
	v_alignbit_b32 v225, v59, v59, 4
	v_pk_fma_f16 v58, v58, s60, v60 op_sel_hi:[1,0,1]
	v_and_b32_e32 v60, 0x7070707, v59
	v_and_b32_e32 v69, 0x7070707, v225
	v_pk_fma_f16 v68, v74, s60, v70 op_sel_hi:[1,0,1]
	v_perm_b32 v60, s2, v205, v60
	v_perm_b32 v69, s2, v205, v69
	v_and_or_b32 v60, v59, s4, v60
	v_and_or_b32 v59, v225, s4, v69
	v_perm_b32 v69, v59, v60, s5
	v_perm_b32 v70, v59, v60, s33
	v_perm_b32 v71, v59, v60, s0
	v_perm_b32 v59, v59, v60, s1
	v_pk_fma_f16 v60, v69, s60, v62 op_sel_hi:[1,0,1]
	v_pk_fma_f16 v62, v70, s60, v64 op_sel_hi:[1,0,1]
	v_pk_fma_f16 v64, v71, s60, v67 op_sel_hi:[1,0,1]
	v_readlane_b32 s36, v120, 48
	v_alignbit_b32 v224, v56, v56, 4
	v_pk_fma_f16 v59, v59, s60, v61 op_sel_hi:[1,0,1]
	v_and_b32_e32 v63, 0x7070707, v56
	v_and_b32_e32 v67, 0x7070707, v224
	v_perm_b32 v63, s2, v205, v63
	v_perm_b32 v67, s2, v205, v67
	v_and_or_b32 v63, v56, s4, v63
	v_and_or_b32 v56, v224, s4, v67
	v_perm_b32 v67, v56, v63, s5
	v_perm_b32 v69, v56, v63, s33
	v_perm_b32 v70, v56, v63, s0
	v_perm_b32 v56, v56, v63, s1
	v_pk_fma_f16 v63, v67, s36, v65 op_sel_hi:[1,0,1]
	v_alignbit_b32 v225, v57, v57, 4
	v_pk_fma_f16 v56, v56, s36, v58 op_sel_hi:[1,0,1]
	v_and_b32_e32 v58, 0x7070707, v57
	v_and_b32_e32 v67, 0x7070707, v225
	v_pk_fma_f16 v65, v69, s36, v66 op_sel_hi:[1,0,1]
	v_pk_fma_f16 v66, v70, s36, v68 op_sel_hi:[1,0,1]
	v_perm_b32 v58, s2, v205, v58
	v_perm_b32 v67, s2, v205, v67
	v_and_or_b32 v58, v57, s4, v58
	v_and_or_b32 v57, v225, s4, v67
	v_perm_b32 v67, v57, v58, s5
	v_perm_b32 v68, v57, v58, s33
	v_perm_b32 v69, v57, v58, s0
	v_perm_b32 v57, v57, v58, s1
	v_pk_fma_f16 v58, v67, s36, v60 op_sel_hi:[1,0,1]
	v_pk_fma_f16 v60, v68, s36, v62 op_sel_hi:[1,0,1]
	v_pk_fma_f16 v62, v69, s36, v64 op_sel_hi:[1,0,1]
	v_readlane_b32 s59, v120, 52
	v_alignbit_b32 v224, v54, v54, 4
	v_pk_fma_f16 v57, v57, s36, v59 op_sel_hi:[1,0,1]
	v_and_b32_e32 v61, 0x7070707, v54
	v_and_b32_e32 v64, 0x7070707, v224
	v_perm_b32 v61, s2, v205, v61
	v_perm_b32 v64, s2, v205, v64
	v_and_or_b32 v61, v54, s4, v61
	v_and_or_b32 v54, v224, s4, v64
	v_perm_b32 v64, v54, v61, s5
	v_perm_b32 v67, v54, v61, s33
	v_perm_b32 v68, v54, v61, s0
	v_perm_b32 v54, v54, v61, s1
	v_pk_fma_f16 v61, v64, s59, v63 op_sel_hi:[1,0,1]
	v_pk_fma_f16 v63, v67, s59, v65 op_sel_hi:[1,0,1]
	v_alignbit_b32 v225, v55, v55, 4
	v_pk_fma_f16 v54, v54, s59, v56 op_sel_hi:[1,0,1]
	v_and_b32_e32 v56, 0x7070707, v55
	v_and_b32_e32 v65, 0x7070707, v225
	v_pk_fma_f16 v64, v68, s59, v66 op_sel_hi:[1,0,1]
	v_perm_b32 v56, s2, v205, v56
	v_perm_b32 v65, s2, v205, v65
	v_and_or_b32 v56, v55, s4, v56
	v_and_or_b32 v55, v225, s4, v65
	v_perm_b32 v65, v55, v56, s5
	v_perm_b32 v66, v55, v56, s33
	v_perm_b32 v67, v55, v56, s0
	v_perm_b32 v55, v55, v56, s1
	v_pk_fma_f16 v56, v65, s59, v58 op_sel_hi:[1,0,1]
	v_pk_fma_f16 v58, v66, s59, v60 op_sel_hi:[1,0,1]
	v_pk_fma_f16 v60, v67, s59, v62 op_sel_hi:[1,0,1]
	v_readlane_b32 s60, v120, 56
	v_alignbit_b32 v224, v52, v52, 4
	v_pk_fma_f16 v55, v55, s59, v57 op_sel_hi:[1,0,1]
	v_and_b32_e32 v59, 0x7070707, v52
	v_and_b32_e32 v62, 0x7070707, v224
	v_perm_b32 v59, s2, v205, v59
	v_perm_b32 v62, s2, v205, v62
	v_and_or_b32 v59, v52, s4, v59
	v_and_or_b32 v52, v224, s4, v62
	v_perm_b32 v62, v52, v59, s5
	v_perm_b32 v65, v52, v59, s33
	v_perm_b32 v66, v52, v59, s0
	v_perm_b32 v52, v52, v59, s1
	v_pk_fma_f16 v59, v62, s60, v61 op_sel_hi:[1,0,1]
	v_pk_fma_f16 v61, v65, s60, v63 op_sel_hi:[1,0,1]
	v_alignbit_b32 v225, v53, v53, 4
	v_pk_fma_f16 v52, v52, s60, v54 op_sel_hi:[1,0,1]
	v_and_b32_e32 v54, 0x7070707, v53
	v_and_b32_e32 v63, 0x7070707, v225
	v_pk_fma_f16 v62, v66, s60, v64 op_sel_hi:[1,0,1]
	v_perm_b32 v54, s2, v205, v54
	v_perm_b32 v63, s2, v205, v63
	v_and_or_b32 v54, v53, s4, v54
	v_and_or_b32 v53, v225, s4, v63
	v_perm_b32 v63, v53, v54, s5
	v_perm_b32 v64, v53, v54, s33
	v_perm_b32 v65, v53, v54, s0
	v_perm_b32 v53, v53, v54, s1
	v_pk_fma_f16 v54, v63, s60, v56 op_sel_hi:[1,0,1]
	v_pk_fma_f16 v56, v64, s60, v58 op_sel_hi:[1,0,1]
	v_pk_fma_f16 v58, v65, s60, v60 op_sel_hi:[1,0,1]
	v_readlane_b32 s36, v120, 60
	v_alignbit_b32 v224, v36, v36, 4
	v_pk_fma_f16 v53, v53, s60, v55 op_sel_hi:[1,0,1]
	v_and_b32_e32 v57, 0x7070707, v36
	v_and_b32_e32 v60, 0x7070707, v224
	v_perm_b32 v57, s2, v205, v57
	v_perm_b32 v60, s2, v205, v60
	v_and_or_b32 v57, v36, s4, v57
	v_and_or_b32 v36, v224, s4, v60
	v_perm_b32 v60, v36, v57, s5
	v_perm_b32 v63, v36, v57, s33
	v_perm_b32 v64, v36, v57, s0
	v_perm_b32 v36, v36, v57, s1
	v_pk_fma_f16 v100, v36, s36, v52 op_sel_hi:[1,0,1]
	v_alignbit_b32 v225, v37, v37, 4
	v_and_b32_e32 v36, 0x7070707, v37
	v_and_b32_e32 v52, 0x7070707, v225
	v_perm_b32 v36, s2, v205, v36
	v_perm_b32 v52, s2, v205, v52
	v_and_or_b32 v36, v37, s4, v36
	v_and_or_b32 v37, v225, s4, v52
	v_pk_fma_f16 v103, v60, s36, v59 op_sel_hi:[1,0,1]
	v_perm_b32 v52, v37, v36, s5
	v_perm_b32 v57, v37, v36, s33
	v_perm_b32 v59, v37, v36, s0
	v_perm_b32 v36, v37, v36, s1
	v_pk_fma_f16 v96, v36, s36, v53 op_sel_hi:[1,0,1]
	s_add_u32 s66, s12, s64
	s_addc_u32 s67, s13, s65
	global_load_dwordx2 v[82:83], v121, s[66:67]
	s_add_u32 s66, s14, s64
	s_addc_u32 s67, s15, s65
	global_load_dwordx2 v[80:81], v121, s[66:67]
	s_add_u32 s66, s38, s62
	s_addc_u32 s67, s39, s63
	global_load_dwordx2 v[48:49], v121, s[66:67]
	s_add_u32 s66, s16, s64
	s_addc_u32 s67, s17, s65
	global_load_dwordx2 v[78:79], v121, s[66:67]
	s_add_u32 s66, s50, s62
	s_addc_u32 s67, s51, s63
	global_load_dwordx2 v[46:47], v121, s[66:67]
	s_add_u32 s66, s18, s64
	s_addc_u32 s67, s19, s65
	global_load_dwordx2 v[76:77], v121, s[66:67]
	s_add_u32 s66, s52, s62
	s_addc_u32 s67, s53, s63
	global_load_dwordx2 v[44:45], v121, s[66:67]
	s_add_u32 s66, s20, s64
	s_addc_u32 s67, s21, s65
	global_load_dwordx2 v[74:75], v121, s[66:67]
	s_add_u32 s66, s54, s62
	s_addc_u32 s67, s55, s63
	global_load_dwordx2 v[42:43], v121, s[66:67]
	s_add_u32 s66, s22, s64
	s_addc_u32 s67, s23, s65
	global_load_dwordx2 v[70:71], v121, s[66:67]
	s_add_u32 s66, s56, s62
	s_addc_u32 s67, s57, s63
	global_load_dwordx2 v[40:41], v121, s[66:67]
	v_pk_fma_f16 v101, v64, s36, v62 op_sel_hi:[1,0,1]
	s_add_u32 s66, s24, s64
	s_addc_u32 s67, s25, s65
	global_load_dwordx2 v[68:69], v121, s[66:67]
	s_add_u32 s66, s26, s64
	s_addc_u32 s67, s27, s65
	global_load_dwordx2 v[64:65], v121, s[66:67]
	v_pk_fma_f16 v102, v63, s36, v61 op_sel_hi:[1,0,1]
	s_add_u32 s66, s28, s64
	s_addc_u32 s67, s29, s65
	global_load_dwordx2 v[62:63], v121, s[66:67]
	s_add_u32 s66, s30, s64
	s_addc_u32 s67, s31, s65
	global_load_dwordx2 v[66:67], v121, s[66:67]
	s_add_u32 s66, s34, s64
	s_addc_u32 s67, s35, s65
	global_load_dwordx2 v[60:61], v121, s[66:67]
	v_pk_fma_f16 v97, v59, s36, v58 op_sel_hi:[1,0,1]
	s_add_u32 s66, s38, s64
	s_addc_u32 s67, s39, s65
	global_load_dwordx2 v[58:59], v121, s[66:67]
	v_pk_fma_f16 v98, v57, s36, v56 op_sel_hi:[1,0,1]
	s_add_u32 s66, s50, s64
	s_addc_u32 s67, s51, s65
	global_load_dwordx2 v[56:57], v121, s[66:67]
	v_pk_fma_f16 v99, v52, s36, v54 op_sel_hi:[1,0,1]
	s_add_u32 s66, s52, s64
	s_addc_u32 s67, s53, s65
	global_load_dwordx2 v[54:55], v121, s[66:67]
	s_add_u32 s66, s54, s64
	s_addc_u32 s67, s55, s65
	global_load_dwordx2 v[52:53], v121, s[66:67]
	s_add_u32 s66, s12, s62
	s_addc_u32 s67, s13, s63
	global_load_dwordx2 v[8:9], v121, s[66:67]
	s_add_u32 s66, s14, s62
	s_addc_u32 s67, s15, s63
	global_load_dwordx2 v[10:11], v121, s[66:67]
	s_nop 0
	s_add_u32 s66, s16, s62
	s_addc_u32 s67, s17, s63
	global_load_dwordx2 v[12:13], v121, s[66:67]
	s_nop 0
	s_add_u32 s66, s18, s62
	s_addc_u32 s67, s19, s63
	global_load_dwordx2 v[14:15], v121, s[66:67]
	s_nop 0
	s_add_u32 s66, s20, s62
	s_addc_u32 s67, s21, s63
	global_load_dwordx2 v[16:17], v121, s[66:67]
	s_nop 0
	s_add_u32 s66, s22, s62
	s_addc_u32 s67, s23, s63
	global_load_dwordx2 v[18:19], v121, s[66:67]
	s_nop 0
	s_add_u32 s66, s24, s62
	s_addc_u32 s67, s25, s63
	global_load_dwordx2 v[20:21], v121, s[66:67]
	s_nop 0
	s_add_u32 s66, s26, s62
	s_addc_u32 s67, s27, s63
	global_load_dwordx2 v[22:23], v121, s[66:67]
	s_nop 0
	s_add_u32 s66, s56, s64
	s_addc_u32 s67, s57, s65
	global_load_dwordx2 v[36:37], v121, s[66:67]
	s_cmpk_eq_i32 s58, 0x90
	s_cbranch_scc0 .LBB0_763
	v_lshlrev_b64 v[0:1], 2, v[2:3]
	v_lshl_add_u64 v[2:3], v[28:29], 0, v[0:1]
	v_mov_b32_e32 v104, v208
	v_mov_b32_e32 v105, v209
	v_mov_b32_e32 v106, v210
	v_mov_b32_e32 v107, v211
	v_mov_b32_e32 v108, v212
	v_mov_b32_e32 v109, v213
	v_mov_b32_e32 v110, v214
	v_mov_b32_e32 v111, v215
	v_mov_b32_e32 v86, v216
	v_mov_b32_e32 v87, v217
	v_mov_b32_e32 v88, v218
	v_mov_b32_e32 v89, v219
	v_mov_b32_e32 v112, v220
	v_mov_b32_e32 v113, v221
	v_mov_b32_e32 v114, v222
	v_mov_b32_e32 v115, v223
	v_lshl_add_u64 v[72:73], v[32:33], 0, v[0:1]
	v_cvt_f32_f16_sdwa v1, v103 dst_sel:DWORD dst_unused:UNUSED_PAD src0_sel:WORD_1
	v_cvt_f32_f16_e32 v0, v103
	v_cvt_f32_f16_sdwa v91, v102 dst_sel:DWORD dst_unused:UNUSED_PAD src0_sel:WORD_1
	v_cvt_f32_f16_e32 v90, v102
	v_cvt_f32_f16_sdwa v103, v101 dst_sel:DWORD dst_unused:UNUSED_PAD src0_sel:WORD_1
	v_cvt_f32_f16_e32 v102, v101
	v_cvt_f32_f16_sdwa v101, v100 dst_sel:DWORD dst_unused:UNUSED_PAD src0_sel:WORD_1
	v_cvt_f32_f16_e32 v100, v100
	s_mov_b32 s18, 0x800000
	v_readlane_b32 s12, v255, 5
	v_readlane_b32 s13, v255, 6
	v_pk_add_f32 v[86:87], v[86:87], v[102:103]
	v_pk_add_f32 v[84:85], v[112:113], v[0:1]
	v_mov_b32_e32 v102, v85
	v_mov_b32_e32 v103, v87
	v_pk_add_f32 v[90:91], v[114:115], v[90:91]
	v_pk_add_f32 v[88:89], v[88:89], v[100:101]
	v_mov_b32_e32 v100, v84
	v_mov_b32_e32 v101, v86
	v_pk_mul_f32 v[102:103], v[102:103], v[102:103]
	v_mov_b32_e32 v112, v91
	v_pk_fma_f32 v[100:101], v[100:101], v[100:101], v[102:103]
	v_mov_b32_e32 v102, v90
	v_mov_b32_e32 v103, v88
	v_pk_fma_f32 v[100:101], v[102:103], v[102:103], v[100:101]
	v_cvt_f32_f16_sdwa v103, v99 dst_sel:DWORD dst_unused:UNUSED_PAD src0_sel:WORD_1
	v_cvt_f32_f16_e32 v102, v99
	v_cvt_f32_f16_sdwa v99, v98 dst_sel:DWORD dst_unused:UNUSED_PAD src0_sel:WORD_1
	v_cvt_f32_f16_e32 v98, v98
	v_mov_b32_e32 v113, v89
	v_pk_add_f32 v[102:103], v[108:109], v[102:103]
	v_cvt_f32_f16_sdwa v109, v97 dst_sel:DWORD dst_unused:UNUSED_PAD src0_sel:WORD_1
	v_cvt_f32_f16_e32 v108, v97
	v_cvt_f32_f16_sdwa v97, v96 dst_sel:DWORD dst_unused:UNUSED_PAD src0_sel:WORD_1
	v_cvt_f32_f16_e32 v96, v96
	v_pk_add_f32 v[98:99], v[110:111], v[98:99]
	v_pk_add_f32 v[104:105], v[104:105], v[108:109]
	v_mov_b32_e32 v108, v103
	v_mov_b32_e32 v109, v105
	v_pk_add_f32 v[96:97], v[106:107], v[96:97]
	v_mov_b32_e32 v106, v102
	v_mov_b32_e32 v107, v104
	v_pk_mul_f32 v[108:109], v[108:109], v[108:109]
	v_pk_fma_f32 v[100:101], v[112:113], v[112:113], v[100:101]
	v_pk_fma_f32 v[106:107], v[106:107], v[106:107], v[108:109]
	v_mov_b32_e32 v108, v98
	v_mov_b32_e32 v109, v96
	v_mov_b32_e32 v110, v99
	v_mov_b32_e32 v111, v97
	v_pk_fma_f32 v[106:107], v[108:109], v[108:109], v[106:107]
	v_add_f32_e32 v95, v100, v101
	v_pk_fma_f32 v[106:107], v[110:111], v[110:111], v[106:107]
	v_lshl_add_u64 v[34:35], v[34:35], 0, s[12:13]
	v_add_f32_e32 v95, v95, v106
	v_add_f32_e32 v95, v95, v107
	v_mov_b32_e32 v100, v95
	s_nop 1
	v_permlane32_swap_b32 v100, v95
	s_waitcnt lgkmcnt(0)
	v_add_f32_e32 v95, v95, v100
	v_mov_b32_e32 v100, v95
	s_nop 1
	v_permlane16_swap_b32 v100, v95
	s_waitcnt lgkmcnt(0)
	v_add_f32_e32 v95, v95, v100
	s_nop 1
	v_mov_b32_dpp v100, v95 row_ror:8 row_mask:0xf bank_mask:0xf
	s_waitcnt lgkmcnt(0)
	v_add_f32_e32 v95, v95, v100
	s_nop 1
	v_mov_b32_dpp v100, v95 row_half_mirror row_mask:0xf bank_mask:0xf
	s_nop 1
	v_mov_b32_dpp v100, v100 quad_perm:[3,2,1,0] row_mask:0xf bank_mask:0xf
	s_waitcnt lgkmcnt(0)
	v_add_f32_e32 v95, v95, v100
	s_nop 1
	v_mov_b32_dpp v100, v95 quad_perm:[2,3,0,1] row_mask:0xf bank_mask:0xf
	s_waitcnt lgkmcnt(0)
	v_add_f32_e32 v95, v95, v100
	s_nop 1
	v_mov_b32_dpp v100, v95 quad_perm:[1,0,3,2] row_mask:0xf bank_mask:0xf
	s_waitcnt lgkmcnt(0)
	v_add_f32_e32 v95, v95, v100
	v_fmamk_f32 v95, v95, 0x3a800000, v191
	v_cmp_gt_f32_e32 vcc, s18, v95
	v_mul_f32_e32 v100, 0x4b800000, v95
	s_nop 0
	v_cndmask_b32_e32 v95, v95, v100, vcc
	v_rsq_f32_e32 v95, v95
	s_nop 0
	v_mul_f32_e32 v100, 0x45800000, v95
	v_cndmask_b32_e32 v100, v95, v100, vcc
	v_pk_mul_f32 v[84:85], v[84:85], v[100:101] op_sel_hi:[1,0]
	v_pk_mul_f32 v[0:1], v[124:125], v[84:85]
	v_pk_mul_f32 v[84:85], v[90:91], v[100:101] op_sel_hi:[1,0]
	s_nop 0
	v_pk_mul_f32 v[2:3], v[126:127], v[84:85]
	global_store_dwordx4 v[72:73], v[0:3], off
	s_nop 1
	v_pk_mul_f32 v[84:85], v[86:87], v[100:101] op_sel_hi:[1,0]
	v_pk_mul_f32 v[0:1], v[128:129], v[84:85]
	v_pk_mul_f32 v[84:85], v[88:89], v[100:101] op_sel_hi:[1,0]
	s_nop 0
	v_pk_mul_f32 v[2:3], v[130:131], v[84:85]
	global_store_dwordx4 v[72:73], v[0:3], off offset:16
	s_nop 1
	v_pk_mul_f32 v[84:85], v[102:103], v[100:101] op_sel_hi:[1,0]
	v_pk_mul_f32 v[0:1], v[84:85], v[132:133]
	v_pk_mul_f32 v[84:85], v[98:99], v[100:101] op_sel_hi:[1,0]
	s_nop 0
	v_pk_mul_f32 v[2:3], v[84:85], v[134:135]
	global_store_dwordx4 v[72:73], v[0:3], off offset:32
	s_nop 1
	v_pk_mul_f32 v[84:85], v[104:105], v[100:101] op_sel_hi:[1,0]
	v_pk_mul_f32 v[0:1], v[84:85], v[136:137]
	v_pk_mul_f32 v[84:85], v[96:97], v[100:101] op_sel_hi:[1,0]
	s_nop 0
	v_pk_mul_f32 v[2:3], v[84:85], v[138:139]
	global_store_dwordx4 v[72:73], v[0:3], off offset:48
	s_nop 1
	v_mov_b32_e32 v0, v94
	s_andn2_b64 exec, exec, s[10:11]
	s_cbranch_execnz .LBB0_762

.LBB0_770:
	s_cmpk_eq_i32 s56, 0x80
	s_cselect_b64 s[10:11], -1, 0
	ds_bpermute_b32 v6, v97, v96
	s_and_b64 vcc, s[10:11], s[48:49]
	v_cndmask_b32_e32 v94, v0, v98, vcc
	v_ashrrev_i32_e32 v95, 31, v94
	s_and_b32 s10, s56, 0x70
	v_lshlrev_b64 v[94:95], 9, v[94:95]
	v_lshl_add_u64 v[94:95], s[94:95], 0, v[94:95]
	s_lshl_b32 s36, s10, 2
	s_waitcnt lgkmcnt(0)
	v_ashrrev_i32_e32 v7, 31, v6
	v_lshl_add_u64 v[94:95], v[94:95], 0, s[36:37]
	v_lshl_add_u64 v[6:7], v[6:7], 3, s[88:89]
	v_lshl_add_u64 v[94:95], v[94:95], 0, v[144:145]
	global_load_dwordx2 v[6:7], v[6:7], off
	s_nop 0
	global_load_dword v8, v[4:5], off
	global_load_dword v96, v[94:95], off
	s_waitcnt vmcnt(33)
	v_dot8_i32_i4 v9, v20, v1, 0
	v_dot8_i32_i4 v94, v20, v10, 0
	v_dot8_i32_i4 v9, v21, v11, v9
	v_dot8_i32_i4 v94, v21, v12, v94
	v_dot8_i32_i4 v20, v22, v1, 0
	v_dot8_i32_i4 v21, v22, v10, 0
	v_dot8_i32_i4 v20, v23, v11, v20
	v_dot8_i32_i4 v21, v23, v12, v21
	v_lshl_add_u32 v9, v9, 4, v94
	s_add_i32 s56, s56, 16
	s_nop 0
	v_lshl_add_u32 v94, v20, 4, v21
	s_waitcnt vmcnt(32)
	v_dot8_i32_i4 v20, v24, v1, 0
	v_dot8_i32_i4 v21, v24, v10, 0
	v_dot8_i32_i4 v20, v25, v11, v20
	v_dot8_i32_i4 v21, v25, v12, v21
	v_lshl_add_u64 v[4:5], v[4:5], 0, 64
	s_waitcnt vmcnt(2)
	v_mul_f32_e32 v7, v13, v7
	v_lshl_add_u32 v95, v20, 4, v21
	v_dot8_i32_i4 v20, v26, v1, 0
	v_dot8_i32_i4 v21, v26, v10, 0
	v_dot8_i32_i4 v20, v27, v11, v20
	v_dot8_i32_i4 v21, v27, v12, v21
	s_waitcnt vmcnt(0)
	v_readlane_b32 s10, v96, 0
	s_ashr_i32 s11, s10, 31
	v_readlane_b32 s12, v96, 1
	v_lshl_add_u32 v106, v20, 4, v21
	v_dot8_i32_i4 v20, v28, v1, 0
	v_dot8_i32_i4 v21, v28, v10, 0
	v_dot8_i32_i4 v20, v29, v11, v20
	v_dot8_i32_i4 v21, v29, v12, v21
	s_lshl_b64 s[10:11], s[10:11], 9
	s_ashr_i32 s13, s12, 31
	v_readlane_b32 s14, v96, 2
	v_lshl_add_u32 v107, v20, 4, v21
	v_dot8_i32_i4 v20, v30, v1, 0
	v_dot8_i32_i4 v21, v30, v10, 0
	v_dot8_i32_i4 v20, v31, v11, v20
	v_dot8_i32_i4 v21, v31, v12, v21
	s_lshl_b64 s[12:13], s[12:13], 9
	s_ashr_i32 s15, s14, 31
	v_readlane_b32 s16, v96, 3
	v_lshl_add_u32 v108, v20, 4, v21
	v_dot8_i32_i4 v20, v32, v1, 0
	v_dot8_i32_i4 v21, v32, v10, 0
	v_dot8_i32_i4 v20, v33, v11, v20
	v_dot8_i32_i4 v21, v33, v12, v21
	s_lshl_b64 s[14:15], s[14:15], 9
	s_ashr_i32 s17, s16, 31
	s_nop 0
	v_lshl_add_u32 v109, v20, 4, v21
	v_dot8_i32_i4 v20, v34, v1, 0
	v_dot8_i32_i4 v21, v34, v10, 0
	v_dot8_i32_i4 v20, v35, v11, v20
	v_dot8_i32_i4 v21, v35, v12, v21
	v_readlane_b32 s18, v96, 4
	s_add_u32 s66, s12, s62
	s_addc_u32 s67, s13, s63
	global_load_dwordx2 v[22:23], v121, s[66:67]
	v_lshl_add_u32 v110, v20, 4, v21
	v_dot8_i32_i4 v20, v36, v1, 0
	v_dot8_i32_i4 v21, v36, v10, 0
	v_dot8_i32_i4 v20, v37, v11, v20
	v_dot8_i32_i4 v21, v37, v12, v21
	s_lshl_b64 s[16:17], s[16:17], 9
	s_ashr_i32 s19, s18, 31
	v_readlane_b32 s20, v96, 5
	v_lshl_add_u32 v111, v20, 4, v21
	v_dot8_i32_i4 v20, v38, v1, 0
	v_dot8_i32_i4 v21, v38, v10, 0
	v_dot8_i32_i4 v20, v39, v11, v20
	v_dot8_i32_i4 v21, v39, v12, v21
	v_permlane32_swap_b32 v9, v111
	s_nop 1
	v_lshl_add_u32 v112, v20, 4, v21
	v_dot8_i32_i4 v20, v40, v1, 0
	v_dot8_i32_i4 v21, v40, v10, 0
	v_dot8_i32_i4 v20, v41, v11, v20
	v_dot8_i32_i4 v21, v41, v12, v21
	s_waitcnt lgkmcnt(0)
	v_add_u32_e32 v9, v9, v111
	v_permlane32_swap_b32 v94, v112
	v_lshl_add_u32 v113, v20, 4, v21
	v_dot8_i32_i4 v20, v60, v1, 0
	v_dot8_i32_i4 v21, v60, v10, 0
	v_dot8_i32_i4 v20, v61, v11, v20
	v_dot8_i32_i4 v21, v61, v12, v21
	s_waitcnt lgkmcnt(0)
	v_add_u32_e32 v94, v94, v112
	v_permlane32_swap_b32 v95, v113
	v_lshl_add_u32 v114, v20, 4, v21
	v_dot8_i32_i4 v20, v58, v1, 0
	v_dot8_i32_i4 v21, v58, v10, 0
	v_dot8_i32_i4 v20, v59, v11, v20
	v_dot8_i32_i4 v21, v59, v12, v21
	s_waitcnt lgkmcnt(0)
	v_add_u32_e32 v95, v95, v113
	v_permlane32_swap_b32 v106, v114
	v_lshl_add_u32 v115, v20, 4, v21
	v_dot8_i32_i4 v20, v56, v1, 0
	v_dot8_i32_i4 v21, v56, v10, 0
	v_dot8_i32_i4 v20, v57, v11, v20
	v_dot8_i32_i4 v21, v57, v12, v21
	s_waitcnt lgkmcnt(0)
	v_add_u32_e32 v106, v106, v114
	v_permlane32_swap_b32 v107, v115
	v_lshl_add_u32 v116, v20, 4, v21
	v_dot8_i32_i4 v20, v54, v1, 0
	v_dot8_i32_i4 v21, v54, v10, 0
	v_dot8_i32_i4 v20, v55, v11, v20
	v_dot8_i32_i4 v21, v55, v12, v21
	s_waitcnt lgkmcnt(0)
	v_add_u32_e32 v107, v107, v115
	v_permlane32_swap_b32 v108, v116
	v_lshl_add_u32 v117, v20, 4, v21
	v_dot8_i32_i4 v20, v52, v1, 0
	v_dot8_i32_i4 v21, v52, v10, 0
	v_dot8_i32_i4 v20, v53, v11, v20
	v_dot8_i32_i4 v21, v53, v12, v21
	s_waitcnt lgkmcnt(0)
	v_add_u32_e32 v108, v108, v116
	v_permlane32_swap_b32 v109, v117
	v_lshl_add_u32 v118, v20, 4, v21
	s_waitcnt lgkmcnt(0)
	v_add_u32_e32 v109, v109, v117
	v_permlane32_swap_b32 v110, v118
	s_add_u32 s66, s10, s62
	s_addc_u32 s67, s11, s63
	global_load_dwordx2 v[20:21], v121, s[66:67]
	s_add_u32 s66, s14, s62
	s_addc_u32 s67, s15, s63
	global_load_dwordx2 v[24:25], v121, s[66:67]
	s_waitcnt lgkmcnt(0)
	v_add_u32_e32 v110, v110, v118
	v_permlane16_swap_b32 v9, v107
	s_lshl_b64 s[18:19], s[18:19], 9
	s_ashr_i32 s21, s20, 31
	v_readlane_b32 s22, v96, 6
	s_add_u32 s66, s16, s62
	s_addc_u32 s67, s17, s63
	global_load_dwordx2 v[26:27], v121, s[66:67]
	s_waitcnt lgkmcnt(0)
	v_add_u32_e32 v9, v9, v107
	v_permlane16_swap_b32 v94, v108
	s_lshl_b64 s[20:21], s[20:21], 9
	s_ashr_i32 s23, s22, 31
	s_waitcnt lgkmcnt(0)
	v_add_u32_e32 v94, v94, v108
	v_permlane16_swap_b32 v95, v109
	v_readlane_b32 s24, v96, 7
	s_add_u32 s66, s18, s62
	s_addc_u32 s67, s19, s63
	global_load_dwordx2 v[28:29], v121, s[66:67]
	s_waitcnt lgkmcnt(0)
	v_add_u32_e32 v95, v95, v109
	v_permlane16_swap_b32 v106, v110
	s_lshl_b64 s[22:23], s[22:23], 9
	s_ashr_i32 s25, s24, 31
	v_readlane_b32 s26, v96, 8
	s_waitcnt lgkmcnt(0)
	v_add_u32_e32 v106, v106, v110
	v_cndmask_b32_e64 v107, v9, v95, s[44:45]
	v_cndmask_b32_e64 v9, v95, v9, s[44:45]
	s_nop 0
	s_add_u32 s66, s20, s62
	s_addc_u32 s67, s21, s63
	global_load_dwordx2 v[30:31], v121, s[66:67]
	s_lshl_b64 s[24:25], s[24:25], 9
	s_ashr_i32 s27, s26, 31
	s_waitcnt lgkmcnt(0)
	v_add_u32_dpp v9, v107, v9 row_ror:8 row_mask:0xf bank_mask:0xf
	v_cndmask_b32_e64 v95, v94, v106, s[44:45]
	s_nop 1
	v_cndmask_b32_e64 v94, v106, v94, s[44:45]
	v_readlane_b32 s28, v96, 9
	s_add_u32 s66, s22, s62
	s_addc_u32 s67, s23, s63
	global_load_dwordx2 v[32:33], v121, s[66:67]
	s_waitcnt lgkmcnt(0)
	v_add_u32_dpp v94, v95, v94 row_ror:8 row_mask:0xf bank_mask:0xf
	v_cndmask_b32_e64 v95, v9, v94, s[46:47]
	v_cndmask_b32_e64 v9, v94, v9, s[46:47]
	s_nop 0
	v_mov_b32_dpp v94, v95 row_half_mirror row_mask:0xf bank_mask:0xf
	s_nop 1
	s_lshl_b64 s[26:27], s[26:27], 9
	s_ashr_i32 s29, s28, 31
	v_readlane_b32 s30, v96, 10
	s_add_u32 s66, s24, s62
	s_addc_u32 s67, s25, s63
	global_load_dwordx2 v[34:35], v121, s[66:67]
	s_waitcnt lgkmcnt(0)
	v_add_u32_dpp v9, v94, v9 quad_perm:[3,2,1,0] row_mask:0xf bank_mask:0xf
	s_nop 1
	s_lshl_b64 s[28:29], s[28:29], 9
	s_ashr_i32 s31, s30, 31
	v_readlane_b32 s34, v96, 11
	s_waitcnt lgkmcnt(0)
	v_add_u32_dpp v9, v9, v9 quad_perm:[2,3,0,1] row_mask:0xf bank_mask:0xf
	s_nop 1
	s_add_u32 s66, s26, s62
	s_addc_u32 s67, s27, s63
	global_load_dwordx2 v[36:37], v121, s[66:67]
	s_lshl_b64 s[30:31], s[30:31], 9
	s_ashr_i32 s35, s34, 31
	s_waitcnt lgkmcnt(0)
	v_add_u32_dpp v9, v9, v9 quad_perm:[1,0,3,2] row_mask:0xf bank_mask:0xf
	v_cvt_f32_i32_e32 v9, v9
	v_add_f32_e32 v9, v14, v9
	v_mul_f32_e32 v7, v7, v9
	v_mul_f32_e32 v9, 0x3d372713, v7
	v_mul_f32_e32 v9, v7, v9
	v_fma_f32 v9, v7, v9, v7
	v_mul_f32_e32 v9, 0x3fcc422a, v9
	v_mul_f32_e32 v9, 0xbfb8aa3b, v9
	v_exp_f32_e32 v9, v9
	v_readlane_b32 s38, v96, 12
	s_add_u32 s66, s28, s62
	s_addc_u32 s67, s29, s63
	global_load_dwordx2 v[38:39], v121, s[66:67]
	v_add_f32_e32 v9, 1.0, v9
	v_rcp_f32_e32 v9, v9
	s_lshl_b64 s[34:35], s[34:35], 9
	s_ashr_i32 s39, s38, 31
	v_pk_mul_f32 v[6:7], v[6:7], v[8:9]
	v_alignbit_b32 v224, v92, v92, 4
	v_pk_mul_f32 v[6:7], v[6:7], v[6:7] op_sel:[0,1] op_sel_hi:[1,0]
	v_cvt_f16_f32_e32 v120, v6
	v_and_b32_e32 v8, 0x7070707, v92
	v_readlane_b32 s36, v120, 0
	v_and_b32_e32 v9, 0x7070707, v224
	v_perm_b32 v8, s2, v205, v8
	v_perm_b32 v9, s2, v205, v9
	v_and_or_b32 v8, v92, s4, v8
	v_and_or_b32 v9, v224, s4, v9
	v_perm_b32 v92, v9, v8, s5
	v_perm_b32 v94, v9, v8, s33
	v_perm_b32 v95, v9, v8, s0
	v_perm_b32 v8, v9, v8, s1
	v_pk_fma_f16 v8, v8, s36, v102 op_sel_hi:[1,0,1]
	v_alignbit_b32 v225, v93, v93, 4
	v_pk_fma_f16 v9, v92, s36, v105 op_sel_hi:[1,0,1]
	v_pk_fma_f16 v92, v94, s36, v104 op_sel_hi:[1,0,1]
	v_pk_fma_f16 v94, v95, s36, v103 op_sel_hi:[1,0,1]
	v_and_b32_e32 v95, 0x7070707, v93
	v_and_b32_e32 v102, 0x7070707, v225
	v_perm_b32 v95, s2, v205, v95
	v_perm_b32 v102, s2, v205, v102
	v_and_or_b32 v95, v93, s4, v95
	v_and_or_b32 v93, v225, s4, v102
	v_perm_b32 v102, v93, v95, s5
	v_perm_b32 v103, v93, v95, s33
	v_perm_b32 v104, v93, v95, s0
	v_perm_b32 v93, v93, v95, s1
	v_pk_fma_f16 v95, v102, s36, v101 op_sel_hi:[1,0,1]
	v_readlane_b32 s59, v120, 4
	v_alignbit_b32 v224, v90, v90, 4
	v_pk_fma_f16 v100, v103, s36, v100 op_sel_hi:[1,0,1]
	v_pk_fma_f16 v99, v104, s36, v99 op_sel_hi:[1,0,1]
	v_pk_fma_f16 v7, v93, s36, v15 op_sel_hi:[1,0,1]
	v_and_b32_e32 v93, 0x7070707, v90
	v_and_b32_e32 v101, 0x7070707, v224
	v_perm_b32 v93, s2, v205, v93
	v_perm_b32 v101, s2, v205, v101
	v_and_or_b32 v93, v90, s4, v93
	v_and_or_b32 v90, v224, s4, v101
	v_perm_b32 v103, v90, v93, s0
	v_perm_b32 v101, v90, v93, s5
	v_perm_b32 v102, v90, v93, s33
	v_perm_b32 v90, v90, v93, s1
	v_pk_fma_f16 v93, v103, s59, v94 op_sel_hi:[1,0,1]
	v_alignbit_b32 v225, v91, v91, 4
	v_pk_fma_f16 v8, v90, s59, v8 op_sel_hi:[1,0,1]
	v_and_b32_e32 v90, 0x7070707, v91
	v_and_b32_e32 v94, 0x7070707, v225
	v_pk_fma_f16 v9, v101, s59, v9 op_sel_hi:[1,0,1]
	v_perm_b32 v90, s2, v205, v90
	v_perm_b32 v94, s2, v205, v94
	v_and_or_b32 v90, v91, s4, v90
	v_and_or_b32 v91, v225, s4, v94
	v_pk_fma_f16 v92, v102, s59, v92 op_sel_hi:[1,0,1]
	v_perm_b32 v94, v91, v90, s5
	v_perm_b32 v102, v91, v90, s0
	v_perm_b32 v101, v91, v90, s33
	v_perm_b32 v90, v91, v90, s1
	v_pk_fma_f16 v91, v94, s59, v95 op_sel_hi:[1,0,1]
	v_pk_fma_f16 v95, v102, s59, v99 op_sel_hi:[1,0,1]
	v_readlane_b32 s60, v120, 8
	v_alignbit_b32 v224, v88, v88, 4
	v_pk_fma_f16 v94, v101, s59, v100 op_sel_hi:[1,0,1]
	v_pk_fma_f16 v7, v90, s59, v7 op_sel_hi:[1,0,1]
	v_and_b32_e32 v90, 0x7070707, v88
	v_and_b32_e32 v99, 0x7070707, v224
	v_perm_b32 v90, s2, v205, v90
	v_perm_b32 v99, s2, v205, v99
	v_and_or_b32 v90, v88, s4, v90
	v_and_or_b32 v88, v224, s4, v99
	v_perm_b32 v100, v88, v90, s33
	v_perm_b32 v101, v88, v90, s0
	v_perm_b32 v99, v88, v90, s5
	v_perm_b32 v88, v88, v90, s1
	v_pk_fma_f16 v90, v100, s60, v92 op_sel_hi:[1,0,1]
	v_pk_fma_f16 v92, v101, s60, v93 op_sel_hi:[1,0,1]
	v_alignbit_b32 v225, v89, v89, 4
	v_pk_fma_f16 v8, v88, s60, v8 op_sel_hi:[1,0,1]
	v_and_b32_e32 v88, 0x7070707, v89
	v_and_b32_e32 v93, 0x7070707, v225
	v_pk_fma_f16 v9, v99, s60, v9 op_sel_hi:[1,0,1]
	v_perm_b32 v88, s2, v205, v88
	v_perm_b32 v93, s2, v205, v93
	v_and_or_b32 v88, v89, s4, v88
	v_and_or_b32 v89, v225, s4, v93
	v_perm_b32 v93, v89, v88, s5
	v_perm_b32 v99, v89, v88, s33
	v_perm_b32 v100, v89, v88, s0
	v_perm_b32 v88, v89, v88, s1
	v_pk_fma_f16 v89, v93, s60, v91 op_sel_hi:[1,0,1]
	v_pk_fma_f16 v91, v99, s60, v94 op_sel_hi:[1,0,1]
	v_readlane_b32 s36, v120, 12
	v_alignbit_b32 v224, v86, v86, 4
	v_pk_fma_f16 v93, v100, s60, v95 op_sel_hi:[1,0,1]
	v_pk_fma_f16 v7, v88, s60, v7 op_sel_hi:[1,0,1]
	v_and_b32_e32 v88, 0x7070707, v86
	v_and_b32_e32 v94, 0x7070707, v224
	v_perm_b32 v88, s2, v205, v88
	v_perm_b32 v94, s2, v205, v94
	v_and_or_b32 v88, v86, s4, v88
	v_and_or_b32 v86, v224, s4, v94
	v_perm_b32 v95, v86, v88, s33
	v_perm_b32 v99, v86, v88, s0
	v_perm_b32 v94, v86, v88, s5
	v_perm_b32 v86, v86, v88, s1
	v_pk_fma_f16 v88, v95, s36, v90 op_sel_hi:[1,0,1]
	v_pk_fma_f16 v90, v99, s36, v92 op_sel_hi:[1,0,1]
	v_alignbit_b32 v225, v87, v87, 4
	v_pk_fma_f16 v8, v86, s36, v8 op_sel_hi:[1,0,1]
	v_and_b32_e32 v86, 0x7070707, v87
	v_and_b32_e32 v92, 0x7070707, v225
	v_pk_fma_f16 v9, v94, s36, v9 op_sel_hi:[1,0,1]
	v_perm_b32 v86, s2, v205, v86
	v_perm_b32 v92, s2, v205, v92
	v_and_or_b32 v86, v87, s4, v86
	v_and_or_b32 v87, v225, s4, v92
	v_perm_b32 v92, v87, v86, s5
	v_perm_b32 v94, v87, v86, s33
	v_perm_b32 v95, v87, v86, s0
	v_perm_b32 v86, v87, v86, s1
	v_pk_fma_f16 v87, v92, s36, v89 op_sel_hi:[1,0,1]
	v_readlane_b32 s59, v120, 16
	v_alignbit_b32 v224, v84, v84, 4
	v_pk_fma_f16 v89, v94, s36, v91 op_sel_hi:[1,0,1]
	v_pk_fma_f16 v91, v95, s36, v93 op_sel_hi:[1,0,1]
	v_pk_fma_f16 v7, v86, s36, v7 op_sel_hi:[1,0,1]
	v_and_b32_e32 v86, 0x7070707, v84
	v_and_b32_e32 v92, 0x7070707, v224
	v_perm_b32 v86, s2, v205, v86
	v_perm_b32 v92, s2, v205, v92
	v_and_or_b32 v86, v84, s4, v86
	v_and_or_b32 v84, v224, s4, v92
	v_perm_b32 v93, v84, v86, s33
	v_perm_b32 v94, v84, v86, s0
	v_perm_b32 v92, v84, v86, s5
	v_perm_b32 v84, v84, v86, s1
	v_pk_fma_f16 v86, v93, s59, v88 op_sel_hi:[1,0,1]
	v_pk_fma_f16 v88, v94, s59, v90 op_sel_hi:[1,0,1]
	v_alignbit_b32 v225, v85, v85, 4
	v_pk_fma_f16 v8, v84, s59, v8 op_sel_hi:[1,0,1]
	v_and_b32_e32 v84, 0x7070707, v85
	v_and_b32_e32 v90, 0x7070707, v225
	v_pk_fma_f16 v9, v92, s59, v9 op_sel_hi:[1,0,1]
	v_perm_b32 v84, s2, v205, v84
	v_perm_b32 v90, s2, v205, v90
	v_and_or_b32 v84, v85, s4, v84
	v_and_or_b32 v85, v225, s4, v90
	v_perm_b32 v90, v85, v84, s5
	v_perm_b32 v92, v85, v84, s33
	v_perm_b32 v93, v85, v84, s0
	v_perm_b32 v84, v85, v84, s1
	v_pk_fma_f16 v85, v90, s59, v87 op_sel_hi:[1,0,1]
	v_readlane_b32 s60, v120, 20
	v_alignbit_b32 v224, v82, v82, 4
	v_pk_fma_f16 v87, v92, s59, v89 op_sel_hi:[1,0,1]
	v_pk_fma_f16 v89, v93, s59, v91 op_sel_hi:[1,0,1]
	v_pk_fma_f16 v7, v84, s59, v7 op_sel_hi:[1,0,1]
	v_and_b32_e32 v84, 0x7070707, v82
	v_and_b32_e32 v90, 0x7070707, v224
	v_perm_b32 v84, s2, v205, v84
	v_perm_b32 v90, s2, v205, v90
	v_and_or_b32 v84, v82, s4, v84
	v_and_or_b32 v82, v224, s4, v90
	v_perm_b32 v91, v82, v84, s33
	v_perm_b32 v92, v82, v84, s0
	v_perm_b32 v90, v82, v84, s5
	v_perm_b32 v82, v82, v84, s1
	v_pk_fma_f16 v84, v91, s60, v86 op_sel_hi:[1,0,1]
	v_pk_fma_f16 v86, v92, s60, v88 op_sel_hi:[1,0,1]
	v_alignbit_b32 v225, v83, v83, 4
	v_pk_fma_f16 v8, v82, s60, v8 op_sel_hi:[1,0,1]
	v_and_b32_e32 v82, 0x7070707, v83
	v_and_b32_e32 v88, 0x7070707, v225
	v_pk_fma_f16 v9, v90, s60, v9 op_sel_hi:[1,0,1]
	v_perm_b32 v82, s2, v205, v82
	v_perm_b32 v88, s2, v205, v88
	v_and_or_b32 v82, v83, s4, v82
	v_and_or_b32 v83, v225, s4, v88
	v_perm_b32 v88, v83, v82, s5
	v_perm_b32 v90, v83, v82, s33
	v_perm_b32 v91, v83, v82, s0
	v_perm_b32 v82, v83, v82, s1
	v_pk_fma_f16 v83, v88, s60, v85 op_sel_hi:[1,0,1]
	v_readlane_b32 s36, v120, 24
	v_alignbit_b32 v224, v80, v80, 4
	v_pk_fma_f16 v85, v90, s60, v87 op_sel_hi:[1,0,1]
	v_pk_fma_f16 v87, v91, s60, v89 op_sel_hi:[1,0,1]
	v_pk_fma_f16 v7, v82, s60, v7 op_sel_hi:[1,0,1]
	v_and_b32_e32 v82, 0x7070707, v80
	v_and_b32_e32 v88, 0x7070707, v224
	v_perm_b32 v82, s2, v205, v82
	v_perm_b32 v88, s2, v205, v88
	v_and_or_b32 v82, v80, s4, v82
	v_and_or_b32 v80, v224, s4, v88
	v_perm_b32 v89, v80, v82, s33
	v_perm_b32 v90, v80, v82, s0
	v_perm_b32 v88, v80, v82, s5
	v_perm_b32 v80, v80, v82, s1
	v_pk_fma_f16 v82, v89, s36, v84 op_sel_hi:[1,0,1]
	v_pk_fma_f16 v84, v90, s36, v86 op_sel_hi:[1,0,1]
	v_alignbit_b32 v225, v81, v81, 4
	v_pk_fma_f16 v8, v80, s36, v8 op_sel_hi:[1,0,1]
	v_and_b32_e32 v80, 0x7070707, v81
	v_and_b32_e32 v86, 0x7070707, v225
	v_pk_fma_f16 v9, v88, s36, v9 op_sel_hi:[1,0,1]
	v_perm_b32 v80, s2, v205, v80
	v_perm_b32 v86, s2, v205, v86
	v_and_or_b32 v80, v81, s4, v80
	v_and_or_b32 v81, v225, s4, v86
	v_perm_b32 v86, v81, v80, s5
	v_perm_b32 v88, v81, v80, s33
	v_perm_b32 v89, v81, v80, s0
	v_perm_b32 v80, v81, v80, s1
	v_pk_fma_f16 v81, v86, s36, v83 op_sel_hi:[1,0,1]
	v_readlane_b32 s59, v120, 28
	v_alignbit_b32 v224, v78, v78, 4
	v_pk_fma_f16 v83, v88, s36, v85 op_sel_hi:[1,0,1]
	v_pk_fma_f16 v85, v89, s36, v87 op_sel_hi:[1,0,1]
	v_pk_fma_f16 v7, v80, s36, v7 op_sel_hi:[1,0,1]
	v_and_b32_e32 v80, 0x7070707, v78
	v_and_b32_e32 v86, 0x7070707, v224
	v_perm_b32 v80, s2, v205, v80
	v_perm_b32 v86, s2, v205, v86
	v_and_or_b32 v80, v78, s4, v80
	v_and_or_b32 v78, v224, s4, v86
	v_perm_b32 v87, v78, v80, s33
	v_perm_b32 v88, v78, v80, s0
	v_perm_b32 v86, v78, v80, s5
	v_perm_b32 v78, v78, v80, s1
	v_pk_fma_f16 v80, v87, s59, v82 op_sel_hi:[1,0,1]
	v_pk_fma_f16 v82, v88, s59, v84 op_sel_hi:[1,0,1]
	v_alignbit_b32 v225, v79, v79, 4
	v_pk_fma_f16 v8, v78, s59, v8 op_sel_hi:[1,0,1]
	v_and_b32_e32 v78, 0x7070707, v79
	v_and_b32_e32 v84, 0x7070707, v225
	v_pk_fma_f16 v9, v86, s59, v9 op_sel_hi:[1,0,1]
	v_perm_b32 v78, s2, v205, v78
	v_perm_b32 v84, s2, v205, v84
	v_and_or_b32 v78, v79, s4, v78
	v_and_or_b32 v79, v225, s4, v84
	v_perm_b32 v84, v79, v78, s5
	v_perm_b32 v86, v79, v78, s33
	v_perm_b32 v87, v79, v78, s0
	v_perm_b32 v78, v79, v78, s1
	v_pk_fma_f16 v79, v84, s59, v81 op_sel_hi:[1,0,1]
	v_readlane_b32 s60, v120, 32
	v_alignbit_b32 v224, v76, v76, 4
	v_pk_fma_f16 v81, v86, s59, v83 op_sel_hi:[1,0,1]
	v_pk_fma_f16 v83, v87, s59, v85 op_sel_hi:[1,0,1]
	v_pk_fma_f16 v7, v78, s59, v7 op_sel_hi:[1,0,1]
	v_and_b32_e32 v78, 0x7070707, v76
	v_and_b32_e32 v84, 0x7070707, v224
	v_perm_b32 v78, s2, v205, v78
	v_perm_b32 v84, s2, v205, v84
	v_and_or_b32 v78, v76, s4, v78
	v_and_or_b32 v76, v224, s4, v84
	v_perm_b32 v85, v76, v78, s33
	v_perm_b32 v86, v76, v78, s0
	v_perm_b32 v84, v76, v78, s5
	v_perm_b32 v76, v76, v78, s1
	v_pk_fma_f16 v78, v85, s60, v80 op_sel_hi:[1,0,1]
	v_pk_fma_f16 v80, v86, s60, v82 op_sel_hi:[1,0,1]
	v_alignbit_b32 v225, v77, v77, 4
	v_pk_fma_f16 v8, v76, s60, v8 op_sel_hi:[1,0,1]
	v_and_b32_e32 v76, 0x7070707, v77
	v_and_b32_e32 v82, 0x7070707, v225
	v_pk_fma_f16 v9, v84, s60, v9 op_sel_hi:[1,0,1]
	v_perm_b32 v76, s2, v205, v76
	v_perm_b32 v82, s2, v205, v82
	v_and_or_b32 v76, v77, s4, v76
	v_and_or_b32 v77, v225, s4, v82
	v_perm_b32 v82, v77, v76, s5
	v_perm_b32 v84, v77, v76, s33
	v_perm_b32 v85, v77, v76, s0
	v_perm_b32 v76, v77, v76, s1
	v_pk_fma_f16 v77, v82, s60, v79 op_sel_hi:[1,0,1]
	v_readlane_b32 s36, v120, 36
	v_alignbit_b32 v224, v70, v70, 4
	v_pk_fma_f16 v79, v84, s60, v81 op_sel_hi:[1,0,1]
	v_pk_fma_f16 v81, v85, s60, v83 op_sel_hi:[1,0,1]
	v_pk_fma_f16 v7, v76, s60, v7 op_sel_hi:[1,0,1]
	v_and_b32_e32 v76, 0x7070707, v70
	v_and_b32_e32 v82, 0x7070707, v224
	v_perm_b32 v76, s2, v205, v76
	v_perm_b32 v82, s2, v205, v82
	v_and_or_b32 v76, v70, s4, v76
	v_and_or_b32 v70, v224, s4, v82
	v_perm_b32 v83, v70, v76, s33
	v_perm_b32 v84, v70, v76, s0
	v_perm_b32 v82, v70, v76, s5
	v_perm_b32 v70, v70, v76, s1
	v_pk_fma_f16 v76, v83, s36, v78 op_sel_hi:[1,0,1]
	v_pk_fma_f16 v78, v84, s36, v80 op_sel_hi:[1,0,1]
	v_alignbit_b32 v225, v71, v71, 4
	v_pk_fma_f16 v8, v70, s36, v8 op_sel_hi:[1,0,1]
	v_and_b32_e32 v70, 0x7070707, v71
	v_and_b32_e32 v80, 0x7070707, v225
	v_pk_fma_f16 v9, v82, s36, v9 op_sel_hi:[1,0,1]
	v_perm_b32 v70, s2, v205, v70
	v_perm_b32 v80, s2, v205, v80
	v_and_or_b32 v70, v71, s4, v70
	v_and_or_b32 v71, v225, s4, v80
	v_perm_b32 v80, v71, v70, s5
	v_perm_b32 v82, v71, v70, s33
	v_perm_b32 v83, v71, v70, s0
	v_perm_b32 v70, v71, v70, s1
	v_pk_fma_f16 v71, v80, s36, v77 op_sel_hi:[1,0,1]
	v_readlane_b32 s59, v120, 40
	v_alignbit_b32 v224, v66, v66, 4
	v_pk_fma_f16 v77, v82, s36, v79 op_sel_hi:[1,0,1]
	v_pk_fma_f16 v79, v83, s36, v81 op_sel_hi:[1,0,1]
	v_pk_fma_f16 v7, v70, s36, v7 op_sel_hi:[1,0,1]
	v_and_b32_e32 v70, 0x7070707, v66
	v_and_b32_e32 v80, 0x7070707, v224
	v_perm_b32 v70, s2, v205, v70
	v_perm_b32 v80, s2, v205, v80
	v_and_or_b32 v70, v66, s4, v70
	v_and_or_b32 v66, v224, s4, v80
	v_perm_b32 v81, v66, v70, s33
	v_perm_b32 v82, v66, v70, s0
	v_perm_b32 v80, v66, v70, s5
	v_perm_b32 v66, v66, v70, s1
	v_pk_fma_f16 v70, v81, s59, v76 op_sel_hi:[1,0,1]
	v_pk_fma_f16 v76, v82, s59, v78 op_sel_hi:[1,0,1]
	v_alignbit_b32 v225, v67, v67, 4
	v_pk_fma_f16 v8, v66, s59, v8 op_sel_hi:[1,0,1]
	v_and_b32_e32 v66, 0x7070707, v67
	v_and_b32_e32 v78, 0x7070707, v225
	v_pk_fma_f16 v9, v80, s59, v9 op_sel_hi:[1,0,1]
	v_perm_b32 v66, s2, v205, v66
	v_perm_b32 v78, s2, v205, v78
	v_and_or_b32 v66, v67, s4, v66
	v_and_or_b32 v67, v225, s4, v78
	v_perm_b32 v78, v67, v66, s5
	v_perm_b32 v80, v67, v66, s33
	v_perm_b32 v81, v67, v66, s0
	v_perm_b32 v66, v67, v66, s1
	v_pk_fma_f16 v67, v78, s59, v71 op_sel_hi:[1,0,1]
	v_readlane_b32 s60, v120, 44
	v_alignbit_b32 v224, v72, v72, 4
	v_pk_fma_f16 v71, v80, s59, v77 op_sel_hi:[1,0,1]
	v_pk_fma_f16 v77, v81, s59, v79 op_sel_hi:[1,0,1]
	v_pk_fma_f16 v7, v66, s59, v7 op_sel_hi:[1,0,1]
	v_and_b32_e32 v66, 0x7070707, v72
	v_and_b32_e32 v78, 0x7070707, v224
	v_perm_b32 v66, s2, v205, v66
	v_perm_b32 v78, s2, v205, v78
	v_and_or_b32 v66, v72, s4, v66
	v_and_or_b32 v72, v224, s4, v78
	v_perm_b32 v80, v72, v66, s0
	v_perm_b32 v78, v72, v66, s5
	v_perm_b32 v79, v72, v66, s33
	v_perm_b32 v66, v72, v66, s1
	v_pk_fma_f16 v72, v80, s60, v76 op_sel_hi:[1,0,1]
	v_alignbit_b32 v225, v73, v73, 4
	v_pk_fma_f16 v8, v66, s60, v8 op_sel_hi:[1,0,1]
	v_and_b32_e32 v66, 0x7070707, v73
	v_and_b32_e32 v76, 0x7070707, v225
	v_pk_fma_f16 v9, v78, s60, v9 op_sel_hi:[1,0,1]
	v_perm_b32 v66, s2, v205, v66
	v_perm_b32 v76, s2, v205, v76
	v_and_or_b32 v66, v73, s4, v66
	v_and_or_b32 v73, v225, s4, v76
	v_perm_b32 v76, v73, v66, s5
	v_pk_fma_f16 v70, v79, s60, v70 op_sel_hi:[1,0,1]
	v_perm_b32 v78, v73, v66, s33
	v_perm_b32 v79, v73, v66, s0
	v_perm_b32 v66, v73, v66, s1
	v_pk_fma_f16 v67, v76, s60, v67 op_sel_hi:[1,0,1]
	v_readlane_b32 s36, v120, 48
	v_alignbit_b32 v224, v68, v68, 4
	v_pk_fma_f16 v71, v78, s60, v71 op_sel_hi:[1,0,1]
	v_pk_fma_f16 v73, v79, s60, v77 op_sel_hi:[1,0,1]
	v_pk_fma_f16 v7, v66, s60, v7 op_sel_hi:[1,0,1]
	v_and_b32_e32 v66, 0x7070707, v68
	v_and_b32_e32 v76, 0x7070707, v224
	v_perm_b32 v66, s2, v205, v66
	v_perm_b32 v76, s2, v205, v76
	v_and_or_b32 v66, v68, s4, v66
	v_and_or_b32 v68, v224, s4, v76
	v_perm_b32 v77, v68, v66, s33
	v_perm_b32 v78, v68, v66, s0
	v_perm_b32 v76, v68, v66, s5
	v_perm_b32 v66, v68, v66, s1
	v_pk_fma_f16 v68, v77, s36, v70 op_sel_hi:[1,0,1]
	v_pk_fma_f16 v70, v78, s36, v72 op_sel_hi:[1,0,1]
	v_alignbit_b32 v225, v69, v69, 4
	v_pk_fma_f16 v8, v66, s36, v8 op_sel_hi:[1,0,1]
	v_and_b32_e32 v66, 0x7070707, v69
	v_and_b32_e32 v72, 0x7070707, v225
	v_pk_fma_f16 v9, v76, s36, v9 op_sel_hi:[1,0,1]
	v_perm_b32 v66, s2, v205, v66
	v_perm_b32 v72, s2, v205, v72
	v_and_or_b32 v66, v69, s4, v66
	v_and_or_b32 v69, v225, s4, v72
	v_perm_b32 v72, v69, v66, s5
	v_perm_b32 v76, v69, v66, s33
	v_perm_b32 v77, v69, v66, s0
	v_perm_b32 v66, v69, v66, s1
	v_pk_fma_f16 v67, v72, s36, v67 op_sel_hi:[1,0,1]
	v_readlane_b32 s59, v120, 52
	v_alignbit_b32 v224, v64, v64, 4
	v_pk_fma_f16 v69, v76, s36, v71 op_sel_hi:[1,0,1]
	v_pk_fma_f16 v71, v77, s36, v73 op_sel_hi:[1,0,1]
	v_pk_fma_f16 v7, v66, s36, v7 op_sel_hi:[1,0,1]
	v_and_b32_e32 v66, 0x7070707, v64
	v_and_b32_e32 v72, 0x7070707, v224
	v_perm_b32 v66, s2, v205, v66
	v_perm_b32 v72, s2, v205, v72
	v_and_or_b32 v66, v64, s4, v66
	v_and_or_b32 v64, v224, s4, v72
	v_perm_b32 v73, v64, v66, s33
	v_perm_b32 v76, v64, v66, s0
	v_perm_b32 v72, v64, v66, s5
	v_perm_b32 v64, v64, v66, s1
	v_pk_fma_f16 v66, v73, s59, v68 op_sel_hi:[1,0,1]
	v_pk_fma_f16 v68, v76, s59, v70 op_sel_hi:[1,0,1]
	v_alignbit_b32 v225, v65, v65, 4
	v_pk_fma_f16 v8, v64, s59, v8 op_sel_hi:[1,0,1]
	v_and_b32_e32 v64, 0x7070707, v65
	v_and_b32_e32 v70, 0x7070707, v225
	v_pk_fma_f16 v9, v72, s59, v9 op_sel_hi:[1,0,1]
	v_perm_b32 v64, s2, v205, v64
	v_perm_b32 v70, s2, v205, v70
	v_and_or_b32 v64, v65, s4, v64
	v_and_or_b32 v65, v225, s4, v70
	v_perm_b32 v70, v65, v64, s5
	v_perm_b32 v72, v65, v64, s33
	v_perm_b32 v73, v65, v64, s0
	v_perm_b32 v64, v65, v64, s1
	v_pk_fma_f16 v65, v70, s59, v67 op_sel_hi:[1,0,1]
	v_readlane_b32 s60, v120, 56
	v_alignbit_b32 v224, v62, v62, 4
	v_pk_fma_f16 v67, v72, s59, v69 op_sel_hi:[1,0,1]
	v_pk_fma_f16 v69, v73, s59, v71 op_sel_hi:[1,0,1]
	v_pk_fma_f16 v7, v64, s59, v7 op_sel_hi:[1,0,1]
	v_and_b32_e32 v64, 0x7070707, v62
	v_and_b32_e32 v70, 0x7070707, v224
	v_perm_b32 v64, s2, v205, v64
	v_perm_b32 v70, s2, v205, v70
	v_and_or_b32 v64, v62, s4, v64
	v_and_or_b32 v62, v224, s4, v70
	v_perm_b32 v71, v62, v64, s33
	v_perm_b32 v72, v62, v64, s0
	v_perm_b32 v70, v62, v64, s5
	v_perm_b32 v62, v62, v64, s1
	v_pk_fma_f16 v64, v71, s60, v66 op_sel_hi:[1,0,1]
	v_pk_fma_f16 v66, v72, s60, v68 op_sel_hi:[1,0,1]
	v_alignbit_b32 v225, v63, v63, 4
	v_pk_fma_f16 v8, v62, s60, v8 op_sel_hi:[1,0,1]
	v_and_b32_e32 v62, 0x7070707, v63
	v_and_b32_e32 v68, 0x7070707, v225
	v_pk_fma_f16 v9, v70, s60, v9 op_sel_hi:[1,0,1]
	v_perm_b32 v62, s2, v205, v62
	v_perm_b32 v68, s2, v205, v68
	v_and_or_b32 v62, v63, s4, v62
	v_and_or_b32 v63, v225, s4, v68
	v_perm_b32 v68, v63, v62, s5
	v_perm_b32 v70, v63, v62, s33
	v_perm_b32 v71, v63, v62, s0
	v_perm_b32 v62, v63, v62, s1
	v_pk_fma_f16 v7, v62, s60, v7 op_sel_hi:[1,0,1]
	v_readlane_b32 s36, v120, 60
	v_alignbit_b32 v224, v50, v50, 4
	v_pk_fma_f16 v63, v68, s60, v65 op_sel_hi:[1,0,1]
	v_pk_fma_f16 v65, v70, s60, v67 op_sel_hi:[1,0,1]
	v_pk_fma_f16 v67, v71, s60, v69 op_sel_hi:[1,0,1]
	v_and_b32_e32 v15, 0x7070707, v50
	v_and_b32_e32 v62, 0x7070707, v224
	v_perm_b32 v15, s2, v205, v15
	v_perm_b32 v62, s2, v205, v62
	v_and_or_b32 v15, v50, s4, v15
	v_and_or_b32 v50, v224, s4, v62
	v_perm_b32 v62, v50, v15, s5
	v_perm_b32 v68, v50, v15, s33
	v_perm_b32 v69, v50, v15, s0
	v_perm_b32 v15, v50, v15, s1
	v_pk_fma_f16 v105, v62, s36, v9 op_sel_hi:[1,0,1]
	v_alignbit_b32 v225, v51, v51, 4
	v_pk_fma_f16 v102, v15, s36, v8 op_sel_hi:[1,0,1]
	v_and_b32_e32 v8, 0x7070707, v51
	v_and_b32_e32 v9, 0x7070707, v225
	v_perm_b32 v8, s2, v205, v8
	v_perm_b32 v9, s2, v205, v9
	v_and_or_b32 v8, v51, s4, v8
	v_and_or_b32 v9, v225, s4, v9
	v_perm_b32 v15, v9, v8, s5
	v_perm_b32 v50, v9, v8, s33
	v_perm_b32 v51, v9, v8, s0
	v_perm_b32 v8, v9, v8, s1
	v_pk_fma_f16 v104, v68, s36, v64 op_sel_hi:[1,0,1]
	v_pk_fma_f16 v103, v69, s36, v66 op_sel_hi:[1,0,1]
	v_pk_fma_f16 v101, v15, s36, v63 op_sel_hi:[1,0,1]
	v_pk_fma_f16 v100, v50, s36, v65 op_sel_hi:[1,0,1]
	v_pk_fma_f16 v99, v51, s36, v67 op_sel_hi:[1,0,1]
	v_pk_fma_f16 v15, v8, s36, v7 op_sel_hi:[1,0,1]
	s_add_u32 s66, s10, s64
	s_addc_u32 s67, s11, s65
	global_load_dwordx2 v[92:93], v121, s[66:67]
	s_add_u32 s66, s12, s64
	s_addc_u32 s67, s13, s65
	global_load_dwordx2 v[90:91], v121, s[66:67]
	s_add_u32 s66, s14, s64
	s_addc_u32 s67, s15, s65
	global_load_dwordx2 v[88:89], v121, s[66:67]
	s_add_u32 s66, s16, s64
	s_addc_u32 s67, s17, s65
	global_load_dwordx2 v[86:87], v121, s[66:67]
	s_add_u32 s66, s18, s64
	s_addc_u32 s67, s19, s65
	global_load_dwordx2 v[84:85], v121, s[66:67]
	s_add_u32 s66, s20, s64
	s_addc_u32 s67, s21, s65
	global_load_dwordx2 v[82:83], v121, s[66:67]
	s_add_u32 s66, s22, s64
	s_addc_u32 s67, s23, s65
	global_load_dwordx2 v[80:81], v121, s[66:67]
	s_add_u32 s66, s24, s64
	s_addc_u32 s67, s25, s65
	global_load_dwordx2 v[78:79], v121, s[66:67]
	s_add_u32 s66, s26, s64
	s_addc_u32 s67, s27, s65
	global_load_dwordx2 v[76:77], v121, s[66:67]
	v_readlane_b32 s50, v96, 13
	s_add_u32 s66, s28, s64
	s_addc_u32 s67, s29, s65
	global_load_dwordx2 v[70:71], v121, s[66:67]
	s_add_u32 s66, s30, s62
	s_addc_u32 s67, s31, s63
	global_load_dwordx2 v[40:41], v121, s[66:67]
	s_lshl_b64 s[38:39], s[38:39], 9
	s_ashr_i32 s51, s50, 31
	v_readlane_b32 s52, v96, 14
	s_add_u32 s66, s30, s64
	s_addc_u32 s67, s31, s65
	global_load_dwordx2 v[66:67], v121, s[66:67]
	s_add_u32 s66, s34, s62
	s_addc_u32 s67, s35, s63
	global_load_dwordx2 v[60:61], v121, s[66:67]
	s_add_u32 s66, s34, s64
	s_addc_u32 s67, s35, s65
	global_load_dwordx2 v[72:73], v121, s[66:67]
	s_lshl_b64 s[50:51], s[50:51], 9
	s_ashr_i32 s53, s52, 31
	v_readlane_b32 s54, v96, 15
	s_add_u32 s66, s38, s62
	s_addc_u32 s67, s39, s63
	global_load_dwordx2 v[58:59], v121, s[66:67]
	s_add_u32 s66, s38, s64
	s_addc_u32 s67, s39, s65
	global_load_dwordx2 v[68:69], v121, s[66:67]
	s_lshl_b64 s[52:53], s[52:53], 9
	s_ashr_i32 s55, s54, 31
	s_add_u32 s66, s50, s62
	s_addc_u32 s67, s51, s63
	global_load_dwordx2 v[56:57], v121, s[66:67]
	s_add_u32 s66, s50, s64
	s_addc_u32 s67, s51, s65
	global_load_dwordx2 v[64:65], v121, s[66:67]
	s_lshl_b64 s[54:55], s[54:55], 9
	s_add_u32 s66, s52, s62
	s_addc_u32 s67, s53, s63
	global_load_dwordx2 v[54:55], v121, s[66:67]
	s_add_u32 s66, s52, s64
	s_addc_u32 s67, s53, s65
	global_load_dwordx2 v[62:63], v121, s[66:67]
	s_add_u32 s66, s54, s62
	s_addc_u32 s67, s55, s63
	global_load_dwordx2 v[52:53], v121, s[66:67]
	s_add_u32 s66, s54, s64
	s_addc_u32 s67, s55, s65
	global_load_dwordx2 v[50:51], v121, s[66:67]
	s_cmpk_eq_i32 s56, 0x90
	s_cbranch_scc0 .LBB0_770
	v_lshl_add_u64 v[94:95], v[2:3], 2, v[44:45]
	v_mov_b32_e32 v106, v208
	v_mov_b32_e32 v107, v209
	v_mov_b32_e32 v108, v210
	v_mov_b32_e32 v109, v211
	v_mov_b32_e32 v8, v212
	v_mov_b32_e32 v9, v213
	v_mov_b32_e32 v10, v214
	v_mov_b32_e32 v11, v215
	v_mov_b32_e32 v4, v216
	v_mov_b32_e32 v5, v217
	v_mov_b32_e32 v6, v218
	v_mov_b32_e32 v7, v219
	v_mov_b32_e32 v0, v220
	v_mov_b32_e32 v1, v221
	v_mov_b32_e32 v2, v222
	v_mov_b32_e32 v3, v223
	v_cvt_f32_f16_sdwa v13, v105 dst_sel:DWORD dst_unused:UNUSED_PAD src0_sel:WORD_1
	v_cvt_f32_f16_e32 v12, v105
	s_mov_b32 s12, 0x800000
	v_readlane_b32 s10, v255, 5
	v_readlane_b32 s11, v255, 6
	v_pk_add_f32 v[0:1], v[0:1], v[12:13]
	v_cvt_f32_f16_sdwa v13, v104 dst_sel:DWORD dst_unused:UNUSED_PAD src0_sel:WORD_1
	v_cvt_f32_f16_e32 v12, v104
	v_lshl_add_u64 v[48:49], v[48:49], 0, s[10:11]
	v_pk_add_f32 v[2:3], v[2:3], v[12:13]
	v_cvt_f32_f16_sdwa v13, v103 dst_sel:DWORD dst_unused:UNUSED_PAD src0_sel:WORD_1
	v_cvt_f32_f16_e32 v12, v103
	global_store_dwordx4 v[94:95], v[0:3], off
	v_pk_add_f32 v[4:5], v[4:5], v[12:13]
	v_cvt_f32_f16_sdwa v13, v102 dst_sel:DWORD dst_unused:UNUSED_PAD src0_sel:WORD_1
	v_cvt_f32_f16_e32 v12, v102
	v_mov_b32_e32 v102, v1
	v_mov_b32_e32 v103, v5
	v_pk_mul_f32 v[102:103], v[102:103], v[102:103]
	v_pk_add_f32 v[6:7], v[6:7], v[12:13]
	v_mov_b32_e32 v12, v0
	v_mov_b32_e32 v13, v4
	v_pk_fma_f32 v[12:13], v[12:13], v[12:13], v[102:103]
	v_mov_b32_e32 v102, v2
	v_mov_b32_e32 v103, v6
	v_pk_fma_f32 v[12:13], v[102:103], v[102:103], v[12:13]
	v_mov_b32_e32 v102, v3
	v_mov_b32_e32 v103, v7
	v_pk_fma_f32 v[102:103], v[102:103], v[102:103], v[12:13]
	v_cvt_f32_f16_sdwa v13, v101 dst_sel:DWORD dst_unused:UNUSED_PAD src0_sel:WORD_1
	v_cvt_f32_f16_e32 v12, v101
	v_cvt_f32_f16_sdwa v101, v15 dst_sel:DWORD dst_unused:UNUSED_PAD src0_sel:WORD_1
	global_store_dwordx4 v[94:95], v[4:7], off offset:16
	v_pk_add_f32 v[8:9], v[8:9], v[12:13]
	v_cvt_f32_f16_sdwa v13, v100 dst_sel:DWORD dst_unused:UNUSED_PAD src0_sel:WORD_1
	v_cvt_f32_f16_e32 v12, v100
	v_cvt_f32_f16_e32 v100, v15
	v_pk_add_f32 v[10:11], v[10:11], v[12:13]
	v_cvt_f32_f16_sdwa v13, v99 dst_sel:DWORD dst_unused:UNUSED_PAD src0_sel:WORD_1
	v_cvt_f32_f16_e32 v12, v99
	v_pk_add_f32 v[14:15], v[108:109], v[100:101]
	v_mov_b32_e32 v100, v9
	global_store_dwordx4 v[94:95], v[8:11], off offset:32
	v_pk_add_f32 v[12:13], v[106:107], v[12:13]
	global_store_dwordx4 v[94:95], v[12:15], off offset:48
	v_mov_b32_e32 v101, v13
	v_mov_b32_e32 v94, v8
	v_mov_b32_e32 v95, v12
	v_pk_mul_f32 v[100:101], v[100:101], v[100:101]
	v_add_f32_e32 v99, v102, v103
	v_pk_fma_f32 v[94:95], v[94:95], v[94:95], v[100:101]
	v_mov_b32_e32 v100, v10
	v_mov_b32_e32 v101, v14
	v_pk_fma_f32 v[94:95], v[100:101], v[100:101], v[94:95]
	v_mov_b32_e32 v100, v11
	v_mov_b32_e32 v101, v15
	v_pk_fma_f32 v[94:95], v[100:101], v[100:101], v[94:95]
	global_load_dwordx4 v[100:103], v[46:47], off offset:48
	global_load_dwordx4 v[104:107], v[46:47], off offset:32
	global_load_dwordx4 v[108:111], v[46:47], off offset:16
	global_load_dwordx4 v[112:115], v[46:47], off
	v_add_f32_e32 v94, v99, v94
	v_add_f32_e32 v94, v94, v95
	v_mov_b32_e32 v95, v94
	s_nop 1
	v_permlane32_swap_b32 v95, v94
	s_waitcnt lgkmcnt(0)
	v_add_f32_e32 v94, v94, v95
	v_mov_b32_e32 v95, v94
	s_nop 1
	v_permlane16_swap_b32 v95, v94
	s_waitcnt lgkmcnt(0)
	v_add_f32_e32 v94, v94, v95
	s_nop 1
	v_mov_b32_dpp v95, v94 row_ror:8 row_mask:0xf bank_mask:0xf
	s_waitcnt lgkmcnt(0)
	v_add_f32_e32 v94, v94, v95
	s_nop 1
	v_mov_b32_dpp v95, v94 row_half_mirror row_mask:0xf bank_mask:0xf
	s_nop 1
	v_mov_b32_dpp v95, v95 quad_perm:[3,2,1,0] row_mask:0xf bank_mask:0xf
	s_waitcnt lgkmcnt(0)
	v_add_f32_e32 v94, v94, v95
	s_nop 1
	v_mov_b32_dpp v95, v94 quad_perm:[2,3,0,1] row_mask:0xf bank_mask:0xf
	s_waitcnt lgkmcnt(0)
	v_add_f32_e32 v94, v94, v95
	s_nop 1
	v_mov_b32_dpp v95, v94 quad_perm:[1,0,3,2] row_mask:0xf bank_mask:0xf
	s_waitcnt lgkmcnt(0)
	v_add_f32_e32 v94, v94, v95
	v_fmamk_f32 v94, v94, 0x3a800000, v191
	v_cmp_gt_f32_e32 vcc, s12, v94
	v_mul_f32_e32 v95, 0x4b800000, v94
	s_nop 0
	v_cndmask_b32_e32 v94, v94, v95, vcc
	v_rsq_f32_e32 v94, v94
	s_nop 0
	v_mul_f32_e32 v95, 0x45800000, v94
	v_cndmask_b32_e32 v94, v94, v95, vcc
	v_pk_mul_f32 v[0:1], v[0:1], v[94:95] op_sel_hi:[1,0]
	v_pk_mul_f32 v[2:3], v[2:3], v[94:95] op_sel_hi:[1,0]
	s_waitcnt vmcnt(0)
	v_pk_mul_f32 v[0:1], v[112:113], v[0:1]
	v_pk_mul_f32 v[2:3], v[114:115], v[2:3]
	v_cvt_pk_bf16_f32 v0, v0, v1
	v_cvt_pk_bf16_f32 v1, v2, v3
	v_pk_mul_f32 v[2:3], v[4:5], v[94:95] op_sel_hi:[1,0]
	v_pk_mul_f32 v[4:5], v[6:7], v[94:95] op_sel_hi:[1,0]
	v_pk_mul_f32 v[2:3], v[108:109], v[2:3]
	v_pk_mul_f32 v[4:5], v[110:111], v[4:5]
	v_cvt_pk_bf16_f32 v2, v2, v3
	v_cvt_pk_bf16_f32 v3, v4, v5
	v_pk_mul_f32 v[4:5], v[8:9], v[94:95] op_sel_hi:[1,0]
	v_pk_mul_f32 v[6:7], v[10:11], v[94:95] op_sel_hi:[1,0]
	v_pk_mul_f32 v[4:5], v[104:105], v[4:5]
	v_pk_mul_f32 v[6:7], v[6:7], v[106:107]
	v_cvt_pk_bf16_f32 v4, v4, v5
	v_cvt_pk_bf16_f32 v5, v6, v7
	v_pk_mul_f32 v[6:7], v[12:13], v[94:95] op_sel_hi:[1,0]
	v_pk_mul_f32 v[8:9], v[14:15], v[94:95] op_sel_hi:[1,0]
	v_pk_mul_f32 v[6:7], v[6:7], v[100:101]
	v_pk_mul_f32 v[8:9], v[8:9], v[102:103]
	v_cvt_pk_bf16_f32 v6, v6, v7
	v_cvt_pk_bf16_f32 v7, v8, v9
	global_store_dwordx4 v[74:75], v[0:3], off
	global_store_dwordx4 v[74:75], v[4:7], off offset:16
	s_nop 0
	v_mov_b32_e32 v0, v98
	s_andn2_b64 exec, exec, s[8:9]
	s_cbranch_execnz .LBB0_769
